# baseline (speedup 1.0000x reference)
.LBB1_3:
	s_load_dwordx8 s[4:11], s[0:1], 0x8
	s_lshr_b32 s16, s13, 6
	s_mul_i32 s14, s16, 0x1800
	s_mov_b32 s15, 0
	s_lshl_b64 s[18:19], s[14:15], 4
	v_and_b32_e32 v2, 63, v0
	s_waitcnt lgkmcnt(0)
	s_lshl_b32 s24, s12, 7
	s_add_u32 s21, s6, s24
	s_add_u32 s22, s8, s24
	s_add_u32 s23, s10, s24
	s_sub_u32 s21, s21, 0x20100
	s_sub_u32 s22, s22, 0x22100
	s_sub_u32 s23, s23, 0x24100
	s_add_u32 s4, s4, s18
	s_addc_u32 s5, s5, s19
	v_lshlrev_b32_e32 v54, 4, v2
	v_mov_b32_e32 v55, 0
	v_lshl_add_u64 v[18:19], s[4:5], 0, v[54:55]
	v_mov_b32_e32 v248, v18
	v_mov_b32_e32 v249, v19
	s_mov_b32 s27, 0
	s_mov_b64 s[28:29], 0x1000
	s_bfe_u32 s4, s2, 0x40003
	s_mul_i32 s14, s4, 0x1800
	v_lshl_add_u64 v[20:21], v[18:19], 0, s[14:15]
	global_load_dwordx4 v[2:5], v[20:21], off offset:2048
	global_load_dwordx4 v[6:9], v[20:21], off
	global_load_dwordx4 v[10:13], v[20:21], off offset:1024
	v_lshrrev_b32_e32 v14, 1, v0
	v_bfe_u32 v56, v0, 4, 2
	v_lshlrev_b32_e32 v54, 7, v1
	v_bitop3_b32 v14, v56, v14, 7 bitop3:0x78
	v_lshl_or_b32 v57, v14, 4, v54
	global_load_dwordx4 v[14:17], v[20:21], off offset:3072
	s_movk_i32 s2, 0x1000
	s_add_i32 s5, s3, 1
	s_and_b32 s5, s5, 15
	v_add_co_u32_e32 v44, vcc, s2, v20
	s_mul_i32 s14, s5, 0x1800
	s_nop 0
	v_addc_co_u32_e32 v45, vcc, 0, v21, vcc
	v_lshl_add_u64 v[46:47], v[18:19], 0, s[14:15]
	global_load_dwordx4 v[20:23], v[44:45], off
	global_load_dwordx4 v[24:27], v[44:45], off offset:1024
	global_load_dwordx4 v[28:31], v[46:47], off
	global_load_dwordx4 v[32:35], v[46:47], off offset:1024
	global_load_dwordx4 v[36:39], v[46:47], off offset:2048
	global_load_dwordx4 v[40:43], v[46:47], off offset:3072
	s_add_i32 s13, s3, 2
	s_and_b32 s13, s13, 15
	v_add_co_u32_e32 v52, vcc, s2, v46
	s_mul_i32 s14, s13, 0x1800
	s_nop 0
	v_addc_co_u32_e32 v53, vcc, 0, v47, vcc
	v_lshl_add_u64 v[58:59], v[18:19], 0, s[14:15]
	global_load_dwordx4 v[44:47], v[52:53], off
	global_load_dwordx4 v[48:51], v[52:53], off offset:1024
	global_load_dwordx4 v[60:63], v[58:59], off
	global_load_dwordx4 v[64:67], v[58:59], off offset:1024
	global_load_dwordx4 v[68:71], v[58:59], off offset:2048
	global_load_dwordx4 v[72:75], v[58:59], off offset:3072
	v_add_co_u32_e32 v52, vcc, s2, v58
	s_add_i32 s5, s3, 3
	s_nop 0
	v_addc_co_u32_e32 v53, vcc, 0, v59, vcc
	global_load_dwordx4 v[76:79], v[52:53], off
	global_load_dwordx4 v[80:83], v[52:53], off offset:1024
	s_add_i32 s26, s3, 3
	s_and_b32 s26, s26, 15
	s_mul_i32 s26, s26, 0x1800
	v_lshl_add_u64 v[250:251], v[248:249], 0, s[26:27]
	global_load_dwordx4 v[176:179], v[250:251], off
	global_load_dwordx4 v[180:183], v[250:251], off offset:1024
	global_load_dwordx4 v[184:187], v[250:251], off offset:2048
	global_load_dwordx4 v[188:191], v[250:251], off offset:3072
	v_lshl_add_u64 v[252:253], v[250:251], 0, s[28:29]
	global_load_dwordx4 v[192:195], v[252:253], off
	global_load_dwordx4 v[196:199], v[252:253], off offset:1024

.Lproj_go_0:
	ds_read_b128 v[84:87], v57
	ds_read_b128 v[88:91], v57 offset:2048
	ds_read_b128 v[96:99], v57 offset:4096
	ds_read_b128 v[104:107], v57 offset:6144
	v_bfe_u32 v52, v0, 1, 3
	v_bitop3_b32 v52, v56, v52, 4 bitop3:0x36
	v_lshl_or_b32 v58, v52, 4, v54
	ds_read_b128 v[124:127], v58
	ds_read_b128 v[128:131], v58 offset:4096
	ds_read_b128 v[132:135], v58 offset:6144
	s_and_b32 s5, s5, 15
	s_mul_i32 s14, s5, 0x1800
	v_lshl_add_u64 v[52:53], v[18:19], 0, s[14:15]
	s_add_i32 s5, s3, 4
	s_and_b32 s5, s5, 15
	s_mul_i32 s14, s5, 0x1800
	s_add_i32 s5, s3, 5
	s_and_b32 s5, s5, 15
	s_xor_b32 s4, s4, 8
	v_or_b32_e32 v59, 0x1a000, v57
	s_ashr_i32 s13, s12, 31
	v_lshl_or_b32 v54, s16, 11, v54
	v_or_b32_e32 v156, s12, v1
	v_ashrrev_i32_e32 v157, 31, v156
	s_waitcnt vmcnt(23) lgkmcnt(6)
	v_mfma_f32_16x16x32_f16 v[92:95], v[84:87], v[2:5], 0
	s_waitcnt lgkmcnt(5)
	v_mfma_f32_16x16x32_f16 v[100:103], v[88:91], v[2:5], 0
	s_waitcnt lgkmcnt(4)
	v_mfma_f32_16x16x32_f16 v[108:111], v[96:99], v[2:5], 0
	s_waitcnt lgkmcnt(3)
	v_mfma_f32_16x16x32_f16 v[2:5], v[104:107], v[2:5], 0
	s_waitcnt vmcnt(22)
	v_mfma_f32_16x16x32_f16 v[112:115], v[6:9], v[84:87], 0
	s_waitcnt vmcnt(21)
	v_mfma_f32_16x16x32_f16 v[84:87], v[10:13], v[84:87], 0
	v_mfma_f32_16x16x32_f16 v[116:119], v[6:9], v[88:91], 0
	v_mfma_f32_16x16x32_f16 v[88:91], v[10:13], v[88:91], 0
	v_mfma_f32_16x16x32_f16 v[120:123], v[6:9], v[96:99], 0
	v_mfma_f32_16x16x32_f16 v[96:99], v[10:13], v[96:99], 0
	v_mfma_f32_16x16x32_f16 v[6:9], v[6:9], v[104:107], 0
	v_mfma_f32_16x16x32_f16 v[10:13], v[10:13], v[104:107], 0
	ds_read_b128 v[104:107], v58 offset:2048
	s_waitcnt vmcnt(18) lgkmcnt(3)
	v_mfma_f32_16x16x32_f16 v[92:95], v[124:127], v[24:27], v[92:95]
	s_waitcnt lgkmcnt(0)
	v_mfma_f32_16x16x32_f16 v[100:103], v[104:107], v[24:27], v[100:103]
	v_mfma_f32_16x16x32_f16 v[108:111], v[128:131], v[24:27], v[108:111]
	v_mfma_f32_16x16x32_f16 v[2:5], v[132:135], v[24:27], v[2:5]
	v_mfma_f32_16x16x32_f16 v[24:27], v[14:17], v[124:127], v[112:115]
	v_mfma_f32_16x16x32_f16 v[84:87], v[20:23], v[124:127], v[84:87]
	v_mfma_f32_16x16x32_f16 v[112:115], v[14:17], v[104:107], v[116:119]
	v_mfma_f32_16x16x32_f16 v[88:91], v[20:23], v[104:107], v[88:91]
	v_mfma_f32_16x16x32_f16 v[104:107], v[14:17], v[128:131], v[120:123]
	v_mfma_f32_16x16x32_f16 v[96:99], v[20:23], v[128:131], v[96:99]
	v_mfma_f32_16x16x32_f16 v[6:9], v[14:17], v[132:135], v[6:9]
	v_mfma_f32_16x16x32_f16 v[10:13], v[20:23], v[132:135], v[10:13]
	v_add_co_u32_e32 v52, vcc, s2, v52
	s_nop 1
	v_addc_co_u32_e32 v53, vcc, 0, v53, vcc
	s_add_i32 s26, s3, 4
	s_and_b32 s26, s26, 15
	s_mul_i32 s26, s26, 0x1800
	v_lshl_add_u64 v[250:251], v[248:249], 0, s[26:27]
	global_load_dwordx4 v[200:203], v[250:251], off
	global_load_dwordx4 v[204:207], v[250:251], off offset:1024
	global_load_dwordx4 v[208:211], v[250:251], off offset:2048
	global_load_dwordx4 v[212:215], v[250:251], off offset:3072
	v_lshl_add_u64 v[252:253], v[250:251], 0, s[28:29]
	global_load_dwordx4 v[216:219], v[252:253], off
	global_load_dwordx4 v[220:223], v[252:253], off offset:1024

.Lproj_go_1:
	ds_read_b128 v[132:135], v57 offset:8192
	ds_read_b128 v[136:139], v57 offset:10240
	s_waitcnt vmcnt(23) lgkmcnt(1)
	v_mfma_f32_16x16x32_f16 v[24:27], v[28:31], v[132:135], v[24:27]
	v_lshl_add_u64 v[52:53], v[18:19], 0, s[14:15]
	s_mul_i32 s14, s5, 0x1800
	s_add_i32 s5, s3, 6
	s_waitcnt vmcnt(22)
	v_mfma_f32_16x16x32_f16 v[84:87], v[32:35], v[132:135], v[84:87]
	s_and_b32 s5, s5, 15
	s_waitcnt vmcnt(21)
	v_mfma_f32_16x16x32_f16 v[92:95], v[132:135], v[36:39], v[92:95]
	s_waitcnt lgkmcnt(0)
	v_mfma_f32_16x16x32_f16 v[112:115], v[28:31], v[136:139], v[112:115]
	v_mfma_f32_16x16x32_f16 v[88:91], v[32:35], v[136:139], v[88:91]
	v_mfma_f32_16x16x32_f16 v[100:103], v[136:139], v[36:39], v[100:103]
	ds_read_b128 v[132:135], v57 offset:12288
	ds_read_b128 v[136:139], v57 offset:14336
	s_waitcnt lgkmcnt(1)
	v_mfma_f32_16x16x32_f16 v[104:107], v[28:31], v[132:135], v[104:107]
	v_mfma_f32_16x16x32_f16 v[96:99], v[32:35], v[132:135], v[96:99]
	s_waitcnt lgkmcnt(0)
	v_mfma_f32_16x16x32_f16 v[6:9], v[28:31], v[136:139], v[6:9]
	v_mfma_f32_16x16x32_f16 v[10:13], v[32:35], v[136:139], v[10:13]
	ds_read_b128 v[28:31], v58 offset:8192
	ds_read_b128 v[32:35], v58 offset:10240
	v_mfma_f32_16x16x32_f16 v[108:111], v[132:135], v[36:39], v[108:111]
	v_mfma_f32_16x16x32_f16 v[2:5], v[136:139], v[36:39], v[2:5]
	s_waitcnt vmcnt(20) lgkmcnt(1)
	v_mfma_f32_16x16x32_f16 v[24:27], v[40:43], v[28:31], v[24:27]
	s_waitcnt vmcnt(19)
	v_mfma_f32_16x16x32_f16 v[36:39], v[44:47], v[28:31], v[84:87]
	s_waitcnt vmcnt(18)
	v_mfma_f32_16x16x32_f16 v[28:31], v[28:31], v[48:51], v[92:95]
	s_waitcnt lgkmcnt(0)
	v_mfma_f32_16x16x32_f16 v[84:87], v[40:43], v[32:35], v[112:115]
	v_mfma_f32_16x16x32_f16 v[88:91], v[44:47], v[32:35], v[88:91]
	v_mfma_f32_16x16x32_f16 v[32:35], v[32:35], v[48:51], v[100:103]
	ds_read_b128 v[92:95], v58 offset:12288
	s_nop 1
	ds_read_b128 v[100:103], v58 offset:14336
	s_waitcnt lgkmcnt(1)
	v_mfma_f32_16x16x32_f16 v[104:107], v[40:43], v[92:95], v[104:107]
	v_mfma_f32_16x16x32_f16 v[96:99], v[44:47], v[92:95], v[96:99]
	v_mfma_f32_16x16x32_f16 v[92:95], v[92:95], v[48:51], v[108:111]
	s_waitcnt lgkmcnt(0)
	v_mfma_f32_16x16x32_f16 v[6:9], v[40:43], v[100:103], v[6:9]
	v_mfma_f32_16x16x32_f16 v[10:13], v[44:47], v[100:103], v[10:13]
	v_mfma_f32_16x16x32_f16 v[2:5], v[100:103], v[48:51], v[2:5]
	v_add_co_u32_e32 v52, vcc, s2, v52
	s_nop 1
	v_addc_co_u32_e32 v53, vcc, 0, v53, vcc
	s_add_i32 s26, s3, 5
	s_and_b32 s26, s26, 15
	s_mul_i32 s26, s26, 0x1800
	v_lshl_add_u64 v[250:251], v[248:249], 0, s[26:27]
	global_load_dwordx4 v[224:227], v[250:251], off
	global_load_dwordx4 v[228:231], v[250:251], off offset:1024
	global_load_dwordx4 v[232:235], v[250:251], off offset:2048
	global_load_dwordx4 v[236:239], v[250:251], off offset:3072
	v_lshl_add_u64 v[252:253], v[250:251], 0, s[28:29]
	global_load_dwordx4 v[240:243], v[252:253], off
	global_load_dwordx4 v[244:247], v[252:253], off offset:1024

.Lproj_go_2:
	ds_read_b128 v[132:135], v57 offset:16384
	ds_read_b128 v[136:139], v57 offset:18432
	s_waitcnt vmcnt(23) lgkmcnt(1)
	v_mfma_f32_16x16x32_f16 v[24:27], v[60:63], v[132:135], v[24:27]
	v_lshl_add_u64 v[52:53], v[18:19], 0, s[14:15]
	s_mul_i32 s14, s5, 0x1800
	s_add_i32 s5, s3, 7
	s_waitcnt vmcnt(22)
	v_mfma_f32_16x16x32_f16 v[36:39], v[64:67], v[132:135], v[36:39]
	s_and_b32 s5, s5, 15
	s_waitcnt vmcnt(21)
	v_mfma_f32_16x16x32_f16 v[28:31], v[132:135], v[68:71], v[28:31]
	s_waitcnt lgkmcnt(0)
	v_mfma_f32_16x16x32_f16 v[84:87], v[60:63], v[136:139], v[84:87]
	v_mfma_f32_16x16x32_f16 v[88:91], v[64:67], v[136:139], v[88:91]
	v_mfma_f32_16x16x32_f16 v[32:35], v[136:139], v[68:71], v[32:35]
	ds_read_b128 v[132:135], v57 offset:20480
	ds_read_b128 v[136:139], v57 offset:22528
	s_waitcnt lgkmcnt(1)
	v_mfma_f32_16x16x32_f16 v[104:107], v[60:63], v[132:135], v[104:107]
	v_mfma_f32_16x16x32_f16 v[96:99], v[64:67], v[132:135], v[96:99]
	s_waitcnt lgkmcnt(0)
	v_mfma_f32_16x16x32_f16 v[6:9], v[60:63], v[136:139], v[6:9]
	v_mfma_f32_16x16x32_f16 v[10:13], v[64:67], v[136:139], v[10:13]
	ds_read_b128 v[60:63], v58 offset:16384
	ds_read_b128 v[64:67], v58 offset:18432
	v_mfma_f32_16x16x32_f16 v[92:95], v[132:135], v[68:71], v[92:95]
	v_mfma_f32_16x16x32_f16 v[2:5], v[136:139], v[68:71], v[2:5]
	s_waitcnt vmcnt(20) lgkmcnt(1)
	v_mfma_f32_16x16x32_f16 v[24:27], v[72:75], v[60:63], v[24:27]
	s_waitcnt vmcnt(19)
	v_mfma_f32_16x16x32_f16 v[36:39], v[76:79], v[60:63], v[36:39]
	s_waitcnt vmcnt(18)
	v_mfma_f32_16x16x32_f16 v[28:31], v[60:63], v[80:83], v[28:31]
	s_waitcnt lgkmcnt(0)
	v_mfma_f32_16x16x32_f16 v[60:63], v[72:75], v[64:67], v[84:87]
	v_mfma_f32_16x16x32_f16 v[68:71], v[76:79], v[64:67], v[88:91]
	v_mfma_f32_16x16x32_f16 v[32:35], v[64:67], v[80:83], v[32:35]
	ds_read_b128 v[64:67], v58 offset:20480
	ds_read_b128 v[84:87], v58 offset:22528
	s_waitcnt lgkmcnt(1)
	v_mfma_f32_16x16x32_f16 v[88:91], v[72:75], v[64:67], v[104:107]
	v_mfma_f32_16x16x32_f16 v[96:99], v[76:79], v[64:67], v[96:99]
	v_mfma_f32_16x16x32_f16 v[64:67], v[64:67], v[80:83], v[92:95]
	s_waitcnt lgkmcnt(0)
	v_mfma_f32_16x16x32_f16 v[6:9], v[72:75], v[84:87], v[6:9]
	v_mfma_f32_16x16x32_f16 v[10:13], v[76:79], v[84:87], v[10:13]
	v_mfma_f32_16x16x32_f16 v[2:5], v[84:87], v[80:83], v[2:5]
	v_add_co_u32_e32 v52, vcc, s2, v52
	s_nop 1
	v_addc_co_u32_e32 v53, vcc, 0, v53, vcc
	s_waitcnt vmcnt(12)
	v_mov_b32_e32 v14, v176
	v_mov_b32_e32 v15, v177
	v_mov_b32_e32 v16, v178
	v_mov_b32_e32 v17, v179
	v_mov_b32_e32 v20, v180
	v_mov_b32_e32 v21, v181
	v_mov_b32_e32 v22, v182
	v_mov_b32_e32 v23, v183
	v_mov_b32_e32 v116, v184
	v_mov_b32_e32 v117, v185
	v_mov_b32_e32 v118, v186
	v_mov_b32_e32 v119, v187
	v_mov_b32_e32 v120, v188
	v_mov_b32_e32 v121, v189
	v_mov_b32_e32 v122, v190
	v_mov_b32_e32 v123, v191
	v_mov_b32_e32 v124, v192
	v_mov_b32_e32 v125, v193
	v_mov_b32_e32 v126, v194
	v_mov_b32_e32 v127, v195
	v_mov_b32_e32 v128, v196
	v_mov_b32_e32 v129, v197
	v_mov_b32_e32 v130, v198
	v_mov_b32_e32 v131, v199
	s_add_i32 s26, s3, 6
	s_and_b32 s26, s26, 15
	s_mul_i32 s26, s26, 0x1800
	v_lshl_add_u64 v[250:251], v[248:249], 0, s[26:27]
	global_load_dwordx4 v[176:179], v[250:251], off
	global_load_dwordx4 v[180:183], v[250:251], off offset:1024
	global_load_dwordx4 v[184:187], v[250:251], off offset:2048
	global_load_dwordx4 v[188:191], v[250:251], off offset:3072
	v_lshl_add_u64 v[252:253], v[250:251], 0, s[28:29]
	global_load_dwordx4 v[192:195], v[252:253], off
	global_load_dwordx4 v[196:199], v[252:253], off offset:1024

.Lproj_go_3:
	ds_read_b128 v[132:135], v57 offset:24576
	ds_read_b128 v[136:139], v57 offset:26624
	s_waitcnt lgkmcnt(1)
	v_mfma_f32_16x16x32_f16 v[24:27], v[14:17], v[132:135], v[24:27]
	v_lshl_add_u64 v[52:53], v[18:19], 0, s[14:15]
	s_mul_i32 s14, s5, 0x1800
	v_mfma_f32_16x16x32_f16 v[36:39], v[20:23], v[132:135], v[36:39]
	v_mfma_f32_16x16x32_f16 v[28:31], v[132:135], v[116:119], v[28:31]
	s_waitcnt lgkmcnt(0)
	v_mfma_f32_16x16x32_f16 v[60:63], v[14:17], v[136:139], v[60:63]
	v_mfma_f32_16x16x32_f16 v[68:71], v[20:23], v[136:139], v[68:71]
	v_mfma_f32_16x16x32_f16 v[32:35], v[136:139], v[116:119], v[32:35]
	ds_read_b128 v[132:135], v57 offset:28672
	ds_read_b128 v[136:139], v57 offset:30720
	s_waitcnt lgkmcnt(1)
	v_mfma_f32_16x16x32_f16 v[88:91], v[14:17], v[132:135], v[88:91]
	v_mfma_f32_16x16x32_f16 v[96:99], v[20:23], v[132:135], v[96:99]
	s_waitcnt lgkmcnt(0)
	v_mfma_f32_16x16x32_f16 v[6:9], v[14:17], v[136:139], v[6:9]
	v_mfma_f32_16x16x32_f16 v[10:13], v[20:23], v[136:139], v[10:13]
	ds_read_b128 v[14:17], v58 offset:24576
	ds_read_b128 v[20:23], v58 offset:26624
	s_waitcnt lgkmcnt(1)
	v_mfma_f32_16x16x32_f16 v[24:27], v[120:123], v[14:17], v[24:27]
	v_mfma_f32_16x16x32_f16 v[36:39], v[124:127], v[14:17], v[36:39]
	v_mfma_f32_16x16x32_f16 v[14:17], v[14:17], v[128:131], v[28:31]
	s_waitcnt lgkmcnt(0)
	v_mfma_f32_16x16x32_f16 v[28:31], v[120:123], v[20:23], v[60:63]
	v_mfma_f32_16x16x32_f16 v[60:63], v[124:127], v[20:23], v[68:71]
	v_mfma_f32_16x16x32_f16 v[20:23], v[20:23], v[128:131], v[32:35]
	s_nop 2
	ds_read_b128 v[32:35], v58 offset:28672
	ds_read_b128 v[68:71], v58 offset:30720
	v_mfma_f32_16x16x32_f16 v[64:67], v[132:135], v[116:119], v[64:67]
	v_mfma_f32_16x16x32_f16 v[2:5], v[136:139], v[116:119], v[2:5]
	s_waitcnt lgkmcnt(1)
	v_mfma_f32_16x16x32_f16 v[88:91], v[120:123], v[32:35], v[88:91]
	v_mfma_f32_16x16x32_f16 v[96:99], v[124:127], v[32:35], v[96:99]
	v_mfma_f32_16x16x32_f16 v[32:35], v[32:35], v[128:131], v[64:67]
	s_waitcnt lgkmcnt(0)
	v_mfma_f32_16x16x32_f16 v[6:9], v[120:123], v[68:71], v[6:9]
	v_mfma_f32_16x16x32_f16 v[10:13], v[124:127], v[68:71], v[10:13]
	v_mfma_f32_16x16x32_f16 v[2:5], v[68:71], v[128:131], v[2:5]
	v_add_co_u32_e32 v52, vcc, s2, v52
	s_nop 1
	v_addc_co_u32_e32 v53, vcc, 0, v53, vcc
	s_waitcnt vmcnt(12)
	v_mov_b32_e32 v40, v200
	v_mov_b32_e32 v41, v201
	v_mov_b32_e32 v42, v202
	v_mov_b32_e32 v43, v203
	v_mov_b32_e32 v44, v204
	v_mov_b32_e32 v45, v205
	v_mov_b32_e32 v46, v206
	v_mov_b32_e32 v47, v207
	v_mov_b32_e32 v48, v208
	v_mov_b32_e32 v49, v209
	v_mov_b32_e32 v50, v210
	v_mov_b32_e32 v51, v211
	v_mov_b32_e32 v100, v212
	v_mov_b32_e32 v101, v213
	v_mov_b32_e32 v102, v214
	v_mov_b32_e32 v103, v215
	v_mov_b32_e32 v108, v216
	v_mov_b32_e32 v109, v217
	v_mov_b32_e32 v110, v218
	v_mov_b32_e32 v111, v219
	v_mov_b32_e32 v112, v220
	v_mov_b32_e32 v113, v221
	v_mov_b32_e32 v114, v222
	v_mov_b32_e32 v115, v223
	s_add_i32 s26, s3, 7
	s_and_b32 s26, s26, 15
	s_mul_i32 s26, s26, 0x1800
	v_lshl_add_u64 v[250:251], v[248:249], 0, s[26:27]
	global_load_dwordx4 v[200:203], v[250:251], off
	global_load_dwordx4 v[204:207], v[250:251], off offset:1024
	global_load_dwordx4 v[208:211], v[250:251], off offset:2048
	global_load_dwordx4 v[212:215], v[250:251], off offset:3072
	v_lshl_add_u64 v[252:253], v[250:251], 0, s[28:29]
	global_load_dwordx4 v[216:219], v[252:253], off
	global_load_dwordx4 v[220:223], v[252:253], off offset:1024

.Lproj_go_4:
	ds_read_b128 v[132:135], v57 offset:32768
	ds_read_b128 v[136:139], v57 offset:34816
	s_waitcnt lgkmcnt(1)
	v_mfma_f32_16x16x32_f16 v[24:27], v[40:43], v[132:135], v[24:27]
	v_lshl_add_u64 v[52:53], v[18:19], 0, s[14:15]
	s_mul_i32 s14, s4, 0x1800
	s_add_i32 s4, s3, 9
	v_mfma_f32_16x16x32_f16 v[36:39], v[44:47], v[132:135], v[36:39]
	s_and_b32 s4, s4, 15
	v_mfma_f32_16x16x32_f16 v[14:17], v[132:135], v[48:51], v[14:17]
	s_waitcnt lgkmcnt(0)
	v_mfma_f32_16x16x32_f16 v[28:31], v[40:43], v[136:139], v[28:31]
	v_mfma_f32_16x16x32_f16 v[60:63], v[44:47], v[136:139], v[60:63]
	v_mfma_f32_16x16x32_f16 v[20:23], v[136:139], v[48:51], v[20:23]
	ds_read_b128 v[132:135], v57 offset:36864
	ds_read_b128 v[136:139], v57 offset:38912
	s_waitcnt lgkmcnt(1)
	v_mfma_f32_16x16x32_f16 v[88:91], v[40:43], v[132:135], v[88:91]
	v_mfma_f32_16x16x32_f16 v[96:99], v[44:47], v[132:135], v[96:99]
	s_waitcnt lgkmcnt(0)
	v_mfma_f32_16x16x32_f16 v[6:9], v[40:43], v[136:139], v[6:9]
	v_mfma_f32_16x16x32_f16 v[10:13], v[44:47], v[136:139], v[10:13]
	ds_read_b128 v[40:43], v58 offset:32768
	ds_read_b128 v[44:47], v58 offset:34816
	v_mfma_f32_16x16x32_f16 v[32:35], v[132:135], v[48:51], v[32:35]
	v_mfma_f32_16x16x32_f16 v[2:5], v[136:139], v[48:51], v[2:5]
	s_waitcnt lgkmcnt(1)
	v_mfma_f32_16x16x32_f16 v[24:27], v[100:103], v[40:43], v[24:27]
	v_mfma_f32_16x16x32_f16 v[36:39], v[108:111], v[40:43], v[36:39]
	v_mfma_f32_16x16x32_f16 v[14:17], v[40:43], v[112:115], v[14:17]
	s_waitcnt lgkmcnt(0)
	v_mfma_f32_16x16x32_f16 v[28:31], v[100:103], v[44:47], v[28:31]
	v_mfma_f32_16x16x32_f16 v[40:43], v[108:111], v[44:47], v[60:63]
	v_mfma_f32_16x16x32_f16 v[20:23], v[44:47], v[112:115], v[20:23]
	ds_read_b128 v[44:47], v58 offset:36864
	ds_read_b128 v[48:51], v58 offset:38912
	s_waitcnt lgkmcnt(1)
	v_mfma_f32_16x16x32_f16 v[60:63], v[100:103], v[44:47], v[88:91]
	v_mfma_f32_16x16x32_f16 v[88:91], v[108:111], v[44:47], v[96:99]
	v_mfma_f32_16x16x32_f16 v[32:35], v[44:47], v[112:115], v[32:35]
	s_waitcnt lgkmcnt(0)
	v_mfma_f32_16x16x32_f16 v[6:9], v[100:103], v[48:51], v[6:9]
	v_mfma_f32_16x16x32_f16 v[10:13], v[108:111], v[48:51], v[10:13]
	v_mfma_f32_16x16x32_f16 v[2:5], v[48:51], v[112:115], v[2:5]
	v_add_co_u32_e32 v52, vcc, s2, v52
	s_nop 1
	v_addc_co_u32_e32 v53, vcc, 0, v53, vcc
	s_waitcnt vmcnt(12)
	v_mov_b32_e32 v72, v224
	v_mov_b32_e32 v73, v225
	v_mov_b32_e32 v74, v226
	v_mov_b32_e32 v75, v227
	v_mov_b32_e32 v76, v228
	v_mov_b32_e32 v77, v229
	v_mov_b32_e32 v78, v230
	v_mov_b32_e32 v79, v231
	v_mov_b32_e32 v80, v232
	v_mov_b32_e32 v81, v233
	v_mov_b32_e32 v82, v234
	v_mov_b32_e32 v83, v235
	v_mov_b32_e32 v84, v236
	v_mov_b32_e32 v85, v237
	v_mov_b32_e32 v86, v238
	v_mov_b32_e32 v87, v239
	v_mov_b32_e32 v92, v240
	v_mov_b32_e32 v93, v241
	v_mov_b32_e32 v94, v242
	v_mov_b32_e32 v95, v243
	v_mov_b32_e32 v104, v244
	v_mov_b32_e32 v105, v245
	v_mov_b32_e32 v106, v246
	v_mov_b32_e32 v107, v247
	s_add_i32 s26, s3, 8
	s_and_b32 s26, s26, 15
	s_mul_i32 s26, s26, 0x1800
	v_lshl_add_u64 v[250:251], v[248:249], 0, s[26:27]
	global_load_dwordx4 v[224:227], v[250:251], off
	global_load_dwordx4 v[228:231], v[250:251], off offset:1024
	global_load_dwordx4 v[232:235], v[250:251], off offset:2048
	global_load_dwordx4 v[236:239], v[250:251], off offset:3072
	v_lshl_add_u64 v[252:253], v[250:251], 0, s[28:29]
	global_load_dwordx4 v[240:243], v[252:253], off
	global_load_dwordx4 v[244:247], v[252:253], off offset:1024

.Lproj_go_5:
	ds_read_b128 v[132:135], v57 offset:40960
	ds_read_b128 v[136:139], v57 offset:43008
	s_waitcnt lgkmcnt(1)
	v_mfma_f32_16x16x32_f16 v[24:27], v[72:75], v[132:135], v[24:27]
	v_lshl_add_u64 v[52:53], v[18:19], 0, s[14:15]
	s_mul_i32 s14, s4, 0x1800
	s_add_i32 s4, s3, 10
	v_mfma_f32_16x16x32_f16 v[36:39], v[76:79], v[132:135], v[36:39]
	s_and_b32 s4, s4, 15
	v_mfma_f32_16x16x32_f16 v[14:17], v[132:135], v[80:83], v[14:17]
	s_waitcnt lgkmcnt(0)
	v_mfma_f32_16x16x32_f16 v[28:31], v[72:75], v[136:139], v[28:31]
	v_mfma_f32_16x16x32_f16 v[40:43], v[76:79], v[136:139], v[40:43]
	v_mfma_f32_16x16x32_f16 v[20:23], v[136:139], v[80:83], v[20:23]
	ds_read_b128 v[132:135], v57 offset:45056
	ds_read_b128 v[136:139], v57 offset:47104
	s_waitcnt lgkmcnt(1)
	v_mfma_f32_16x16x32_f16 v[60:63], v[72:75], v[132:135], v[60:63]
	v_mfma_f32_16x16x32_f16 v[88:91], v[76:79], v[132:135], v[88:91]
	s_waitcnt lgkmcnt(0)
	v_mfma_f32_16x16x32_f16 v[6:9], v[72:75], v[136:139], v[6:9]
	v_mfma_f32_16x16x32_f16 v[10:13], v[76:79], v[136:139], v[10:13]
	ds_read_b128 v[72:75], v58 offset:40960
	ds_read_b128 v[76:79], v58 offset:43008
	s_waitcnt lgkmcnt(1)
	v_mfma_f32_16x16x32_f16 v[24:27], v[84:87], v[72:75], v[24:27]
	v_mfma_f32_16x16x32_f16 v[36:39], v[92:95], v[72:75], v[36:39]
	v_mfma_f32_16x16x32_f16 v[14:17], v[72:75], v[104:107], v[14:17]
	s_waitcnt lgkmcnt(0)
	v_mfma_f32_16x16x32_f16 v[28:31], v[84:87], v[76:79], v[28:31]
	v_mfma_f32_16x16x32_f16 v[40:43], v[92:95], v[76:79], v[40:43]
	v_mfma_f32_16x16x32_f16 v[20:23], v[76:79], v[104:107], v[20:23]
	ds_read_b128 v[72:75], v58 offset:45056
	ds_read_b128 v[76:79], v58 offset:47104
	v_mfma_f32_16x16x32_f16 v[32:35], v[132:135], v[80:83], v[32:35]
	v_mfma_f32_16x16x32_f16 v[2:5], v[136:139], v[80:83], v[2:5]
	s_waitcnt lgkmcnt(1)
	v_mfma_f32_16x16x32_f16 v[60:63], v[84:87], v[72:75], v[60:63]
	v_mfma_f32_16x16x32_f16 v[80:83], v[92:95], v[72:75], v[88:91]
	v_mfma_f32_16x16x32_f16 v[32:35], v[72:75], v[104:107], v[32:35]
	s_waitcnt lgkmcnt(0)
	v_mfma_f32_16x16x32_f16 v[6:9], v[84:87], v[76:79], v[6:9]
	v_mfma_f32_16x16x32_f16 v[10:13], v[92:95], v[76:79], v[10:13]
	v_mfma_f32_16x16x32_f16 v[2:5], v[76:79], v[104:107], v[2:5]
	v_add_co_u32_e32 v52, vcc, s2, v52
	s_nop 1
	v_addc_co_u32_e32 v53, vcc, 0, v53, vcc
	s_waitcnt vmcnt(12)
	v_mov_b32_e32 v64, v176
	v_mov_b32_e32 v65, v177
	v_mov_b32_e32 v66, v178
	v_mov_b32_e32 v67, v179
	v_mov_b32_e32 v68, v180
	v_mov_b32_e32 v69, v181
	v_mov_b32_e32 v70, v182
	v_mov_b32_e32 v71, v183
	v_mov_b32_e32 v116, v184
	v_mov_b32_e32 v117, v185
	v_mov_b32_e32 v118, v186
	v_mov_b32_e32 v119, v187
	v_mov_b32_e32 v120, v188
	v_mov_b32_e32 v121, v189
	v_mov_b32_e32 v122, v190
	v_mov_b32_e32 v123, v191
	v_mov_b32_e32 v124, v192
	v_mov_b32_e32 v125, v193
	v_mov_b32_e32 v126, v194
	v_mov_b32_e32 v127, v195
	v_mov_b32_e32 v128, v196
	v_mov_b32_e32 v129, v197
	v_mov_b32_e32 v130, v198
	v_mov_b32_e32 v131, v199
	s_add_i32 s26, s3, 9
	s_and_b32 s26, s26, 15
	s_mul_i32 s26, s26, 0x1800
	v_lshl_add_u64 v[250:251], v[248:249], 0, s[26:27]
	global_load_dwordx4 v[176:179], v[250:251], off
	global_load_dwordx4 v[180:183], v[250:251], off offset:1024
	global_load_dwordx4 v[184:187], v[250:251], off offset:2048
	global_load_dwordx4 v[188:191], v[250:251], off offset:3072
	v_lshl_add_u64 v[252:253], v[250:251], 0, s[28:29]
	global_load_dwordx4 v[192:195], v[252:253], off
	global_load_dwordx4 v[196:199], v[252:253], off offset:1024

.Lproj_go_6:
	ds_read_b128 v[132:135], v57 offset:49152
	ds_read_b128 v[136:139], v57 offset:51200
	s_waitcnt lgkmcnt(1)
	v_mfma_f32_16x16x32_f16 v[24:27], v[64:67], v[132:135], v[24:27]
	v_lshl_add_u64 v[52:53], v[18:19], 0, s[14:15]
	s_mul_i32 s14, s4, 0x1800
	s_add_i32 s4, s3, 11
	v_mfma_f32_16x16x32_f16 v[36:39], v[68:71], v[132:135], v[36:39]
	s_and_b32 s4, s4, 15
	v_mfma_f32_16x16x32_f16 v[14:17], v[132:135], v[116:119], v[14:17]
	s_waitcnt lgkmcnt(0)
	v_mfma_f32_16x16x32_f16 v[28:31], v[64:67], v[136:139], v[28:31]
	v_mfma_f32_16x16x32_f16 v[40:43], v[68:71], v[136:139], v[40:43]
	v_mfma_f32_16x16x32_f16 v[20:23], v[136:139], v[116:119], v[20:23]
	ds_read_b128 v[132:135], v57 offset:53248
	ds_read_b128 v[136:139], v57 offset:55296
	s_waitcnt lgkmcnt(1)
	v_mfma_f32_16x16x32_f16 v[60:63], v[64:67], v[132:135], v[60:63]
	v_mfma_f32_16x16x32_f16 v[80:83], v[68:71], v[132:135], v[80:83]
	s_waitcnt lgkmcnt(0)
	v_mfma_f32_16x16x32_f16 v[6:9], v[64:67], v[136:139], v[6:9]
	v_mfma_f32_16x16x32_f16 v[10:13], v[68:71], v[136:139], v[10:13]
	ds_read_b128 v[64:67], v58 offset:49152
	ds_read_b128 v[68:71], v58 offset:51200
	s_waitcnt lgkmcnt(1)
	v_mfma_f32_16x16x32_f16 v[24:27], v[120:123], v[64:67], v[24:27]
	v_mfma_f32_16x16x32_f16 v[36:39], v[124:127], v[64:67], v[36:39]
	v_mfma_f32_16x16x32_f16 v[14:17], v[64:67], v[128:131], v[14:17]
	s_waitcnt lgkmcnt(0)
	v_mfma_f32_16x16x32_f16 v[28:31], v[120:123], v[68:71], v[28:31]
	v_mfma_f32_16x16x32_f16 v[40:43], v[124:127], v[68:71], v[40:43]
	v_mfma_f32_16x16x32_f16 v[20:23], v[68:71], v[128:131], v[20:23]
	ds_read_b128 v[64:67], v58 offset:53248
	ds_read_b128 v[68:71], v58 offset:55296
	v_mfma_f32_16x16x32_f16 v[32:35], v[132:135], v[116:119], v[32:35]
	v_mfma_f32_16x16x32_f16 v[2:5], v[136:139], v[116:119], v[2:5]
	s_waitcnt lgkmcnt(1)
	v_mfma_f32_16x16x32_f16 v[60:63], v[120:123], v[64:67], v[60:63]
	v_mfma_f32_16x16x32_f16 v[80:83], v[124:127], v[64:67], v[80:83]
	v_mfma_f32_16x16x32_f16 v[32:35], v[64:67], v[128:131], v[32:35]
	s_waitcnt lgkmcnt(0)
	v_mfma_f32_16x16x32_f16 v[6:9], v[120:123], v[68:71], v[6:9]
	v_mfma_f32_16x16x32_f16 v[10:13], v[124:127], v[68:71], v[10:13]
	v_mfma_f32_16x16x32_f16 v[2:5], v[68:71], v[128:131], v[2:5]
	v_add_co_u32_e32 v52, vcc, s2, v52
	s_nop 1
	v_addc_co_u32_e32 v53, vcc, 0, v53, vcc
	s_waitcnt vmcnt(12)
	v_mov_b32_e32 v44, v200
	v_mov_b32_e32 v45, v201
	v_mov_b32_e32 v46, v202
	v_mov_b32_e32 v47, v203
	v_mov_b32_e32 v48, v204
	v_mov_b32_e32 v49, v205
	v_mov_b32_e32 v50, v206
	v_mov_b32_e32 v51, v207
	v_mov_b32_e32 v96, v208
	v_mov_b32_e32 v97, v209
	v_mov_b32_e32 v98, v210
	v_mov_b32_e32 v99, v211
	v_mov_b32_e32 v100, v212
	v_mov_b32_e32 v101, v213
	v_mov_b32_e32 v102, v214
	v_mov_b32_e32 v103, v215
	v_mov_b32_e32 v108, v216
	v_mov_b32_e32 v109, v217
	v_mov_b32_e32 v110, v218
	v_mov_b32_e32 v111, v219
	v_mov_b32_e32 v112, v220
	v_mov_b32_e32 v113, v221
	v_mov_b32_e32 v114, v222
	v_mov_b32_e32 v115, v223
	s_add_i32 s26, s3, 10
	s_and_b32 s26, s26, 15
	s_mul_i32 s26, s26, 0x1800
	v_lshl_add_u64 v[250:251], v[248:249], 0, s[26:27]
	global_load_dwordx4 v[200:203], v[250:251], off
	global_load_dwordx4 v[204:207], v[250:251], off offset:1024
	global_load_dwordx4 v[208:211], v[250:251], off offset:2048
	global_load_dwordx4 v[212:215], v[250:251], off offset:3072
	v_lshl_add_u64 v[252:253], v[250:251], 0, s[28:29]
	global_load_dwordx4 v[216:219], v[252:253], off
	global_load_dwordx4 v[220:223], v[252:253], off offset:1024

.Lproj_go_7:
	ds_read_b128 v[132:135], v57 offset:57344
	ds_read_b128 v[136:139], v57 offset:59392
	s_waitcnt lgkmcnt(1)
	v_mfma_f32_16x16x32_f16 v[24:27], v[44:47], v[132:135], v[24:27]
	v_lshl_add_u64 v[52:53], v[18:19], 0, s[14:15]
	s_mul_i32 s14, s4, 0x1800
	s_add_i32 s4, s3, 12
	v_mfma_f32_16x16x32_f16 v[36:39], v[48:51], v[132:135], v[36:39]
	s_and_b32 s4, s4, 15
	v_mfma_f32_16x16x32_f16 v[14:17], v[132:135], v[96:99], v[14:17]
	s_waitcnt lgkmcnt(0)
	v_mfma_f32_16x16x32_f16 v[28:31], v[44:47], v[136:139], v[28:31]
	v_mfma_f32_16x16x32_f16 v[40:43], v[48:51], v[136:139], v[40:43]
	v_mfma_f32_16x16x32_f16 v[20:23], v[136:139], v[96:99], v[20:23]
	ds_read_b128 v[132:135], v57 offset:61440
	ds_read_b128 v[136:139], v57 offset:63488
	s_waitcnt lgkmcnt(1)
	v_mfma_f32_16x16x32_f16 v[60:63], v[44:47], v[132:135], v[60:63]
	v_mfma_f32_16x16x32_f16 v[80:83], v[48:51], v[132:135], v[80:83]
	s_waitcnt lgkmcnt(0)
	v_mfma_f32_16x16x32_f16 v[6:9], v[44:47], v[136:139], v[6:9]
	v_mfma_f32_16x16x32_f16 v[10:13], v[48:51], v[136:139], v[10:13]
	ds_read_b128 v[44:47], v58 offset:57344
	ds_read_b128 v[48:51], v58 offset:59392
	s_waitcnt lgkmcnt(1)
	v_mfma_f32_16x16x32_f16 v[24:27], v[100:103], v[44:47], v[24:27]
	v_mfma_f32_16x16x32_f16 v[36:39], v[108:111], v[44:47], v[36:39]
	v_mfma_f32_16x16x32_f16 v[14:17], v[44:47], v[112:115], v[14:17]
	s_waitcnt lgkmcnt(0)
	v_mfma_f32_16x16x32_f16 v[28:31], v[100:103], v[48:51], v[28:31]
	v_mfma_f32_16x16x32_f16 v[40:43], v[108:111], v[48:51], v[40:43]
	v_mfma_f32_16x16x32_f16 v[20:23], v[48:51], v[112:115], v[20:23]
	ds_read_b128 v[44:47], v58 offset:61440
	ds_read_b128 v[48:51], v58 offset:63488
	v_mfma_f32_16x16x32_f16 v[32:35], v[132:135], v[96:99], v[32:35]
	v_mfma_f32_16x16x32_f16 v[2:5], v[136:139], v[96:99], v[2:5]
	s_waitcnt lgkmcnt(1)
	v_mfma_f32_16x16x32_f16 v[60:63], v[100:103], v[44:47], v[60:63]
	v_mfma_f32_16x16x32_f16 v[80:83], v[108:111], v[44:47], v[80:83]
	v_mfma_f32_16x16x32_f16 v[32:35], v[44:47], v[112:115], v[32:35]
	s_waitcnt lgkmcnt(0)
	v_mfma_f32_16x16x32_f16 v[6:9], v[100:103], v[48:51], v[6:9]
	v_mfma_f32_16x16x32_f16 v[10:13], v[108:111], v[48:51], v[10:13]
	v_mfma_f32_16x16x32_f16 v[2:5], v[48:51], v[112:115], v[2:5]
	v_add_co_u32_e32 v52, vcc, s2, v52
	s_nop 1
	v_addc_co_u32_e32 v53, vcc, 0, v53, vcc
	v_or_b32_e32 v52, 0x10000, v57
	s_waitcnt vmcnt(12)
	v_mov_b32_e32 v72, v224
	v_mov_b32_e32 v73, v225
	v_mov_b32_e32 v74, v226
	v_mov_b32_e32 v75, v227
	v_mov_b32_e32 v76, v228
	v_mov_b32_e32 v77, v229
	v_mov_b32_e32 v78, v230
	v_mov_b32_e32 v79, v231
	v_mov_b32_e32 v84, v232
	v_mov_b32_e32 v85, v233
	v_mov_b32_e32 v86, v234
	v_mov_b32_e32 v87, v235
	v_mov_b32_e32 v88, v236
	v_mov_b32_e32 v89, v237
	v_mov_b32_e32 v90, v238
	v_mov_b32_e32 v91, v239
	v_mov_b32_e32 v92, v240
	v_mov_b32_e32 v93, v241
	v_mov_b32_e32 v94, v242
	v_mov_b32_e32 v95, v243
	v_mov_b32_e32 v104, v244
	v_mov_b32_e32 v105, v245
	v_mov_b32_e32 v106, v246
	v_mov_b32_e32 v107, v247
	s_add_i32 s26, s3, 11
	s_and_b32 s26, s26, 15
	s_mul_i32 s26, s26, 0x1800
	v_lshl_add_u64 v[250:251], v[248:249], 0, s[26:27]
	global_load_dwordx4 v[224:227], v[250:251], off
	global_load_dwordx4 v[228:231], v[250:251], off offset:1024
	global_load_dwordx4 v[232:235], v[250:251], off offset:2048
	global_load_dwordx4 v[236:239], v[250:251], off offset:3072
	v_lshl_add_u64 v[252:253], v[250:251], 0, s[28:29]
	global_load_dwordx4 v[240:243], v[252:253], off
	global_load_dwordx4 v[244:247], v[252:253], off offset:1024

.Lproj_go_8:
	ds_read_b128 v[132:135], v52
	v_or_b32_e32 v52, 0x10800, v57
	ds_read_b128 v[136:139], v52
	v_or_b32_e32 v52, 0x11000, v57
	s_waitcnt lgkmcnt(1)
	v_mfma_f32_16x16x32_f16 v[24:27], v[72:75], v[132:135], v[24:27]
	v_mfma_f32_16x16x32_f16 v[36:39], v[76:79], v[132:135], v[36:39]
	v_mfma_f32_16x16x32_f16 v[14:17], v[132:135], v[84:87], v[14:17]
	ds_read_b128 v[132:135], v52
	v_or_b32_e32 v52, 0x11800, v57
	s_waitcnt lgkmcnt(1)
	v_mfma_f32_16x16x32_f16 v[28:31], v[72:75], v[136:139], v[28:31]
	v_mfma_f32_16x16x32_f16 v[40:43], v[76:79], v[136:139], v[40:43]
	v_mfma_f32_16x16x32_f16 v[20:23], v[136:139], v[84:87], v[20:23]
	ds_read_b128 v[136:139], v52
	v_or_b32_e32 v52, 0x10000, v58
	s_waitcnt lgkmcnt(1)
	v_mfma_f32_16x16x32_f16 v[60:63], v[72:75], v[132:135], v[60:63]
	s_waitcnt lgkmcnt(0)
	v_mfma_f32_16x16x32_f16 v[6:9], v[72:75], v[136:139], v[6:9]
	ds_read_b128 v[72:75], v52
	v_or_b32_e32 v52, 0x10800, v58
	v_mfma_f32_16x16x32_f16 v[80:83], v[76:79], v[132:135], v[80:83]
	v_mfma_f32_16x16x32_f16 v[10:13], v[76:79], v[136:139], v[10:13]
	ds_read_b128 v[76:79], v52
	v_or_b32_e32 v52, 0x11000, v58
	s_waitcnt lgkmcnt(1)
	v_mfma_f32_16x16x32_f16 v[24:27], v[88:91], v[72:75], v[24:27]
	v_mfma_f32_16x16x32_f16 v[36:39], v[92:95], v[72:75], v[36:39]
	v_mfma_f32_16x16x32_f16 v[14:17], v[72:75], v[104:107], v[14:17]
	ds_read_b128 v[72:75], v52
	v_or_b32_e32 v52, 0x11800, v58
	s_waitcnt lgkmcnt(1)
	v_mfma_f32_16x16x32_f16 v[28:31], v[88:91], v[76:79], v[28:31]
	v_mfma_f32_16x16x32_f16 v[40:43], v[92:95], v[76:79], v[40:43]
	v_mfma_f32_16x16x32_f16 v[20:23], v[76:79], v[104:107], v[20:23]
	ds_read_b128 v[76:79], v52
	v_lshl_add_u64 v[52:53], v[18:19], 0, s[14:15]
	s_mul_i32 s14, s4, 0x1800
	v_mfma_f32_16x16x32_f16 v[32:35], v[132:135], v[84:87], v[32:35]
	s_add_i32 s4, s3, 13
	s_and_b32 s4, s4, 15
	v_mfma_f32_16x16x32_f16 v[2:5], v[136:139], v[84:87], v[2:5]
	s_waitcnt lgkmcnt(1)
	v_mfma_f32_16x16x32_f16 v[60:63], v[88:91], v[72:75], v[60:63]
	v_mfma_f32_16x16x32_f16 v[80:83], v[92:95], v[72:75], v[80:83]
	v_mfma_f32_16x16x32_f16 v[32:35], v[72:75], v[104:107], v[32:35]
	s_waitcnt lgkmcnt(0)
	v_mfma_f32_16x16x32_f16 v[6:9], v[88:91], v[76:79], v[6:9]
	v_mfma_f32_16x16x32_f16 v[10:13], v[92:95], v[76:79], v[10:13]
	v_mfma_f32_16x16x32_f16 v[2:5], v[76:79], v[104:107], v[2:5]
	v_add_co_u32_e32 v52, vcc, s2, v52
	s_nop 1
	v_addc_co_u32_e32 v53, vcc, 0, v53, vcc
	v_or_b32_e32 v52, 0x12000, v57
	s_waitcnt vmcnt(12)
	v_mov_b32_e32 v64, v176
	v_mov_b32_e32 v65, v177
	v_mov_b32_e32 v66, v178
	v_mov_b32_e32 v67, v179
	v_mov_b32_e32 v68, v180
	v_mov_b32_e32 v69, v181
	v_mov_b32_e32 v70, v182
	v_mov_b32_e32 v71, v183
	v_mov_b32_e32 v116, v184
	v_mov_b32_e32 v117, v185
	v_mov_b32_e32 v118, v186
	v_mov_b32_e32 v119, v187
	v_mov_b32_e32 v120, v188
	v_mov_b32_e32 v121, v189
	v_mov_b32_e32 v122, v190
	v_mov_b32_e32 v123, v191
	v_mov_b32_e32 v124, v192
	v_mov_b32_e32 v125, v193
	v_mov_b32_e32 v126, v194
	v_mov_b32_e32 v127, v195
	v_mov_b32_e32 v128, v196
	v_mov_b32_e32 v129, v197
	v_mov_b32_e32 v130, v198
	v_mov_b32_e32 v131, v199
	s_add_i32 s26, s3, 12
	s_and_b32 s26, s26, 15
	s_mul_i32 s26, s26, 0x1800
	v_lshl_add_u64 v[250:251], v[248:249], 0, s[26:27]
	global_load_dwordx4 v[176:179], v[250:251], off
	global_load_dwordx4 v[180:183], v[250:251], off offset:1024
	global_load_dwordx4 v[184:187], v[250:251], off offset:2048
	global_load_dwordx4 v[188:191], v[250:251], off offset:3072
	v_lshl_add_u64 v[252:253], v[250:251], 0, s[28:29]
	global_load_dwordx4 v[192:195], v[252:253], off
	global_load_dwordx4 v[196:199], v[252:253], off offset:1024

.Lproj_go_9:
	ds_read_b128 v[132:135], v52
	v_or_b32_e32 v52, 0x12800, v57
	ds_read_b128 v[136:139], v52
	v_or_b32_e32 v52, 0x13000, v57
	s_waitcnt lgkmcnt(1)
	v_mfma_f32_16x16x32_f16 v[24:27], v[64:67], v[132:135], v[24:27]
	v_mfma_f32_16x16x32_f16 v[36:39], v[68:71], v[132:135], v[36:39]
	v_mfma_f32_16x16x32_f16 v[14:17], v[132:135], v[116:119], v[14:17]
	ds_read_b128 v[132:135], v52
	v_or_b32_e32 v52, 0x13800, v57
	s_waitcnt lgkmcnt(1)
	v_mfma_f32_16x16x32_f16 v[28:31], v[64:67], v[136:139], v[28:31]
	v_mfma_f32_16x16x32_f16 v[40:43], v[68:71], v[136:139], v[40:43]
	v_mfma_f32_16x16x32_f16 v[20:23], v[136:139], v[116:119], v[20:23]
	ds_read_b128 v[136:139], v52
	v_or_b32_e32 v52, 0x12000, v58
	s_waitcnt lgkmcnt(1)
	v_mfma_f32_16x16x32_f16 v[60:63], v[64:67], v[132:135], v[60:63]
	s_waitcnt lgkmcnt(0)
	v_mfma_f32_16x16x32_f16 v[6:9], v[64:67], v[136:139], v[6:9]
	ds_read_b128 v[64:67], v52
	v_or_b32_e32 v52, 0x12800, v58
	v_mfma_f32_16x16x32_f16 v[80:83], v[68:71], v[132:135], v[80:83]
	v_mfma_f32_16x16x32_f16 v[10:13], v[68:71], v[136:139], v[10:13]
	ds_read_b128 v[68:71], v52
	v_or_b32_e32 v52, 0x13000, v58
	s_waitcnt lgkmcnt(1)
	v_mfma_f32_16x16x32_f16 v[24:27], v[120:123], v[64:67], v[24:27]
	v_mfma_f32_16x16x32_f16 v[36:39], v[124:127], v[64:67], v[36:39]
	v_mfma_f32_16x16x32_f16 v[14:17], v[64:67], v[128:131], v[14:17]
	ds_read_b128 v[64:67], v52
	v_or_b32_e32 v52, 0x13800, v58
	s_waitcnt lgkmcnt(1)
	v_mfma_f32_16x16x32_f16 v[28:31], v[120:123], v[68:71], v[28:31]
	v_mfma_f32_16x16x32_f16 v[40:43], v[124:127], v[68:71], v[40:43]
	v_mfma_f32_16x16x32_f16 v[20:23], v[68:71], v[128:131], v[20:23]
	ds_read_b128 v[68:71], v52
	v_lshl_add_u64 v[52:53], v[18:19], 0, s[14:15]
	s_mul_i32 s14, s4, 0x1800
	v_mfma_f32_16x16x32_f16 v[32:35], v[132:135], v[116:119], v[32:35]
	s_add_i32 s4, s3, 14
	s_and_b32 s4, s4, 15
	v_mfma_f32_16x16x32_f16 v[2:5], v[136:139], v[116:119], v[2:5]
	s_waitcnt lgkmcnt(1)
	v_mfma_f32_16x16x32_f16 v[60:63], v[120:123], v[64:67], v[60:63]
	v_mfma_f32_16x16x32_f16 v[80:83], v[124:127], v[64:67], v[80:83]
	v_mfma_f32_16x16x32_f16 v[32:35], v[64:67], v[128:131], v[32:35]
	s_waitcnt lgkmcnt(0)
	v_mfma_f32_16x16x32_f16 v[6:9], v[120:123], v[68:71], v[6:9]
	v_mfma_f32_16x16x32_f16 v[10:13], v[124:127], v[68:71], v[10:13]
	v_mfma_f32_16x16x32_f16 v[2:5], v[68:71], v[128:131], v[2:5]
	v_add_co_u32_e32 v52, vcc, s2, v52
	s_nop 1
	v_addc_co_u32_e32 v53, vcc, 0, v53, vcc
	v_or_b32_e32 v52, 0x14000, v57
	s_waitcnt vmcnt(12)
	v_mov_b32_e32 v44, v200
	v_mov_b32_e32 v45, v201
	v_mov_b32_e32 v46, v202
	v_mov_b32_e32 v47, v203
	v_mov_b32_e32 v48, v204
	v_mov_b32_e32 v49, v205
	v_mov_b32_e32 v50, v206
	v_mov_b32_e32 v51, v207
	v_mov_b32_e32 v96, v208
	v_mov_b32_e32 v97, v209
	v_mov_b32_e32 v98, v210
	v_mov_b32_e32 v99, v211
	v_mov_b32_e32 v100, v212
	v_mov_b32_e32 v101, v213
	v_mov_b32_e32 v102, v214
	v_mov_b32_e32 v103, v215
	v_mov_b32_e32 v108, v216
	v_mov_b32_e32 v109, v217
	v_mov_b32_e32 v110, v218
	v_mov_b32_e32 v111, v219
	v_mov_b32_e32 v112, v220
	v_mov_b32_e32 v113, v221
	v_mov_b32_e32 v114, v222
	v_mov_b32_e32 v115, v223
	s_add_i32 s26, s3, 13
	s_and_b32 s26, s26, 15
	s_mul_i32 s26, s26, 0x1800
	v_lshl_add_u64 v[250:251], v[248:249], 0, s[26:27]
	global_load_dwordx4 v[200:203], v[250:251], off
	global_load_dwordx4 v[204:207], v[250:251], off offset:1024
	global_load_dwordx4 v[208:211], v[250:251], off offset:2048
	global_load_dwordx4 v[212:215], v[250:251], off offset:3072
	v_lshl_add_u64 v[252:253], v[250:251], 0, s[28:29]
	global_load_dwordx4 v[216:219], v[252:253], off
	global_load_dwordx4 v[220:223], v[252:253], off offset:1024

.Lproj_go_10:
	ds_read_b128 v[132:135], v52
	v_or_b32_e32 v52, 0x14800, v57
	ds_read_b128 v[136:139], v52
	v_or_b32_e32 v52, 0x15000, v57
	s_waitcnt lgkmcnt(1)
	v_mfma_f32_16x16x32_f16 v[24:27], v[44:47], v[132:135], v[24:27]
	v_mfma_f32_16x16x32_f16 v[36:39], v[48:51], v[132:135], v[36:39]
	v_mfma_f32_16x16x32_f16 v[14:17], v[132:135], v[96:99], v[14:17]
	ds_read_b128 v[132:135], v52
	v_or_b32_e32 v52, 0x15800, v57
	s_waitcnt lgkmcnt(1)
	v_mfma_f32_16x16x32_f16 v[28:31], v[44:47], v[136:139], v[28:31]
	v_mfma_f32_16x16x32_f16 v[40:43], v[48:51], v[136:139], v[40:43]
	v_mfma_f32_16x16x32_f16 v[20:23], v[136:139], v[96:99], v[20:23]
	ds_read_b128 v[136:139], v52
	s_waitcnt lgkmcnt(1)
	v_mfma_f32_16x16x32_f16 v[60:63], v[44:47], v[132:135], v[60:63]
	s_waitcnt lgkmcnt(0)
	v_mfma_f32_16x16x32_f16 v[6:9], v[44:47], v[136:139], v[6:9]
	v_or_b32_e32 v44, 0x14000, v58
	ds_read_b128 v[44:47], v44
	v_mfma_f32_16x16x32_f16 v[80:83], v[48:51], v[132:135], v[80:83]
	v_mfma_f32_16x16x32_f16 v[10:13], v[48:51], v[136:139], v[10:13]
	v_or_b32_e32 v48, 0x14800, v58
	ds_read_b128 v[48:51], v48
	s_waitcnt lgkmcnt(1)
	v_mfma_f32_16x16x32_f16 v[24:27], v[100:103], v[44:47], v[24:27]
	v_mfma_f32_16x16x32_f16 v[36:39], v[108:111], v[44:47], v[36:39]
	v_mfma_f32_16x16x32_f16 v[14:17], v[44:47], v[112:115], v[14:17]
	v_or_b32_e32 v44, 0x15000, v58
	ds_read_b128 v[44:47], v44
	s_waitcnt lgkmcnt(1)
	v_mfma_f32_16x16x32_f16 v[28:31], v[100:103], v[48:51], v[28:31]
	v_mfma_f32_16x16x32_f16 v[40:43], v[108:111], v[48:51], v[40:43]
	v_mfma_f32_16x16x32_f16 v[20:23], v[48:51], v[112:115], v[20:23]
	v_or_b32_e32 v48, 0x15800, v58
	ds_read_b128 v[48:51], v48
	v_mfma_f32_16x16x32_f16 v[32:35], v[132:135], v[96:99], v[32:35]
	v_mfma_f32_16x16x32_f16 v[2:5], v[136:139], v[96:99], v[2:5]
	s_waitcnt lgkmcnt(1)
	v_mfma_f32_16x16x32_f16 v[60:63], v[100:103], v[44:47], v[60:63]
	v_mfma_f32_16x16x32_f16 v[80:83], v[108:111], v[44:47], v[80:83]
	v_mfma_f32_16x16x32_f16 v[32:35], v[44:47], v[112:115], v[32:35]
	v_lshl_add_u64 v[44:45], v[18:19], 0, s[14:15]
	s_mul_i32 s14, s4, 0x1800
	s_add_i32 s4, s3, -1
	s_waitcnt lgkmcnt(0)
	v_mfma_f32_16x16x32_f16 v[6:9], v[100:103], v[48:51], v[6:9]
	s_and_b32 s4, s4, 15
	v_mfma_f32_16x16x32_f16 v[10:13], v[108:111], v[48:51], v[10:13]
	v_mfma_f32_16x16x32_f16 v[2:5], v[48:51], v[112:115], v[2:5]
	v_add_co_u32_e32 v44, vcc, s2, v44
	v_or_b32_e32 v48, 0x16800, v57
	s_nop 0
	v_addc_co_u32_e32 v45, vcc, 0, v45, vcc
	v_or_b32_e32 v44, 0x16000, v57
	s_waitcnt vmcnt(12)
	v_mov_b32_e32 v72, v224
	v_mov_b32_e32 v73, v225
	v_mov_b32_e32 v74, v226
	v_mov_b32_e32 v75, v227
	v_mov_b32_e32 v76, v228
	v_mov_b32_e32 v77, v229
	v_mov_b32_e32 v78, v230
	v_mov_b32_e32 v79, v231
	v_mov_b32_e32 v84, v232
	v_mov_b32_e32 v85, v233
	v_mov_b32_e32 v86, v234
	v_mov_b32_e32 v87, v235
	v_mov_b32_e32 v88, v236
	v_mov_b32_e32 v89, v237
	v_mov_b32_e32 v90, v238
	v_mov_b32_e32 v91, v239
	v_mov_b32_e32 v92, v240
	v_mov_b32_e32 v93, v241
	v_mov_b32_e32 v94, v242
	v_mov_b32_e32 v95, v243
	v_mov_b32_e32 v104, v244
	v_mov_b32_e32 v105, v245
	v_mov_b32_e32 v106, v246
	v_mov_b32_e32 v107, v247
	s_add_i32 s26, s3, 14
	s_and_b32 s26, s26, 15
	s_mul_i32 s26, s26, 0x1800
	v_lshl_add_u64 v[250:251], v[248:249], 0, s[26:27]
	global_load_dwordx4 v[224:227], v[250:251], off
	global_load_dwordx4 v[228:231], v[250:251], off offset:1024
	global_load_dwordx4 v[232:235], v[250:251], off offset:2048
	global_load_dwordx4 v[236:239], v[250:251], off offset:3072
	v_lshl_add_u64 v[252:253], v[250:251], 0, s[28:29]
	global_load_dwordx4 v[240:243], v[252:253], off
	global_load_dwordx4 v[244:247], v[252:253], off offset:1024

.Lproj_go_11:
	ds_read_b128 v[44:47], v44
	ds_read_b128 v[136:139], v48
	s_waitcnt lgkmcnt(1)
	v_mfma_f32_16x16x32_f16 v[24:27], v[72:75], v[44:47], v[24:27]
	v_or_b32_e32 v48, 0x17800, v57
	v_mfma_f32_16x16x32_f16 v[36:39], v[76:79], v[44:47], v[36:39]
	v_mfma_f32_16x16x32_f16 v[14:17], v[44:47], v[84:87], v[14:17]
	v_or_b32_e32 v44, 0x17000, v57
	ds_read_b128 v[44:47], v44
	s_waitcnt lgkmcnt(1)
	v_mfma_f32_16x16x32_f16 v[28:31], v[72:75], v[136:139], v[28:31]
	v_mfma_f32_16x16x32_f16 v[40:43], v[76:79], v[136:139], v[40:43]
	v_mfma_f32_16x16x32_f16 v[20:23], v[136:139], v[84:87], v[20:23]
	ds_read_b128 v[136:139], v48
	v_or_b32_e32 v48, 0x16800, v58
	s_waitcnt lgkmcnt(1)
	v_mfma_f32_16x16x32_f16 v[60:63], v[72:75], v[44:47], v[60:63]
	v_mfma_f32_16x16x32_f16 v[80:83], v[76:79], v[44:47], v[80:83]
	v_mfma_f32_16x16x32_f16 v[32:35], v[44:47], v[84:87], v[32:35]
	v_or_b32_e32 v44, 0x16000, v58
	ds_read_b128 v[44:47], v44
	s_waitcnt lgkmcnt(1)
	v_mfma_f32_16x16x32_f16 v[6:9], v[72:75], v[136:139], v[6:9]
	ds_read_b128 v[72:75], v48
	v_mfma_f32_16x16x32_f16 v[10:13], v[76:79], v[136:139], v[10:13]
	v_mfma_f32_16x16x32_f16 v[2:5], v[136:139], v[84:87], v[2:5]
	s_waitcnt lgkmcnt(1)
	v_mfma_f32_16x16x32_f16 v[76:79], v[44:47], v[104:107], v[14:17]
	s_waitcnt lgkmcnt(0)
	v_mfma_f32_16x16x32_f16 v[84:87], v[92:95], v[72:75], v[40:43]
	s_nop 0
	v_or_b32_e32 v14, 0x17000, v58
	ds_read_b128 v[14:17], v14
	v_or_b32_e32 v40, 0x17800, v58
	ds_read_b128 v[40:43], v40
	v_mfma_f32_16x16x32_f16 v[24:27], v[88:91], v[44:47], v[24:27]
	v_mfma_f32_16x16x32_f16 v[36:39], v[92:95], v[44:47], v[36:39]
	v_mfma_f32_16x16x32_f16 v[28:31], v[88:91], v[72:75], v[28:31]
	v_mfma_f32_16x16x32_f16 v[20:23], v[72:75], v[104:107], v[20:23]
	s_waitcnt lgkmcnt(1)
	v_mfma_f32_16x16x32_f16 v[60:63], v[88:91], v[14:17], v[60:63]
	v_mfma_f32_16x16x32_f16 v[72:75], v[92:95], v[14:17], v[80:83]
	s_waitcnt lgkmcnt(0)
	v_mfma_f32_16x16x32_f16 v[80:83], v[88:91], v[40:43], v[6:9]
	v_mfma_f32_16x16x32_f16 v[88:91], v[92:95], v[40:43], v[10:13]
	v_mfma_f32_16x16x32_f16 v[92:95], v[40:43], v[104:107], v[2:5]
	v_or_b32_e32 v40, 0x18000, v57
	s_nop 1
	v_lshl_add_u64 v[2:3], v[18:19], 0, s[14:15]
	v_mfma_f32_16x16x32_f16 v[32:35], v[14:17], v[104:107], v[32:35]
	v_add_co_u32_e32 v2, vcc, s2, v2
	s_mul_i32 s14, s4, 0x1800
	s_nop 0
	v_addc_co_u32_e32 v3, vcc, 0, v3, vcc
	s_nop 0
	s_waitcnt vmcnt(12)
	v_mov_b32_e32 v64, v176
	v_mov_b32_e32 v65, v177
	v_mov_b32_e32 v66, v178
	v_mov_b32_e32 v67, v179
	v_mov_b32_e32 v68, v180
	v_mov_b32_e32 v69, v181
	v_mov_b32_e32 v70, v182
	v_mov_b32_e32 v71, v183
	v_mov_b32_e32 v116, v184
	v_mov_b32_e32 v117, v185
	v_mov_b32_e32 v118, v186
	v_mov_b32_e32 v119, v187
	v_mov_b32_e32 v120, v188
	v_mov_b32_e32 v121, v189
	v_mov_b32_e32 v122, v190
	v_mov_b32_e32 v123, v191
	v_mov_b32_e32 v124, v192
	v_mov_b32_e32 v125, v193
	v_mov_b32_e32 v126, v194
	v_mov_b32_e32 v127, v195
	v_mov_b32_e32 v128, v196
	v_mov_b32_e32 v129, v197
	v_mov_b32_e32 v130, v198
	v_mov_b32_e32 v131, v199
	s_add_i32 s26, s3, 15
	s_and_b32 s26, s26, 15
	s_mul_i32 s26, s26, 0x1800
	v_lshl_add_u64 v[250:251], v[248:249], 0, s[26:27]
	global_load_dwordx4 v[176:179], v[250:251], off
	global_load_dwordx4 v[180:183], v[250:251], off offset:1024
	global_load_dwordx4 v[184:187], v[250:251], off offset:2048
	global_load_dwordx4 v[188:191], v[250:251], off offset:3072
	v_lshl_add_u64 v[252:253], v[250:251], 0, s[28:29]
	global_load_dwordx4 v[192:195], v[252:253], off
	global_load_dwordx4 v[196:199], v[252:253], off offset:1024

.Lproj_go_12:
	ds_read_b128 v[104:107], v40
	v_or_b32_e32 v40, 0x18800, v57
	ds_read_b128 v[136:139], v40
	v_or_b32_e32 v40, 0x19000, v57
	s_waitcnt lgkmcnt(1)
	v_mfma_f32_16x16x32_f16 v[24:27], v[64:67], v[104:107], v[24:27]
	v_lshl_add_u64 v[18:19], v[18:19], 0, s[14:15]
	s_lshl_b64 s[4:5], s[12:13], 7
	s_add_u32 s4, s10, s4
	v_mfma_f32_16x16x32_f16 v[36:39], v[68:71], v[104:107], v[36:39]
	s_addc_u32 s5, s11, s5
	v_mfma_f32_16x16x32_f16 v[76:79], v[104:107], v[116:119], v[76:79]
	ds_read_b128 v[104:107], v40
	v_or_b32_e32 v40, 0x19800, v57
	s_waitcnt lgkmcnt(1)
	v_mfma_f32_16x16x32_f16 v[28:31], v[64:67], v[136:139], v[28:31]
	v_mfma_f32_16x16x32_f16 v[84:87], v[68:71], v[136:139], v[84:87]
	v_mfma_f32_16x16x32_f16 v[20:23], v[136:139], v[116:119], v[20:23]
	ds_read_b128 v[136:139], v40
	v_or_b32_e32 v40, 0x18000, v58
	s_waitcnt lgkmcnt(1)
	v_mfma_f32_16x16x32_f16 v[72:75], v[68:71], v[104:107], v[72:75]
	s_waitcnt lgkmcnt(0)
	v_mfma_f32_16x16x32_f16 v[68:71], v[68:71], v[136:139], v[88:91]
	s_nop 2
	ds_read_b128 v[88:91], v40
	v_or_b32_e32 v40, 0x18800, v58
	v_mfma_f32_16x16x32_f16 v[60:63], v[64:67], v[104:107], v[60:63]
	v_mfma_f32_16x16x32_f16 v[64:67], v[64:67], v[136:139], v[80:83]
	v_mfma_f32_16x16x32_f16 v[80:83], v[136:139], v[116:119], v[92:95]
	s_nop 2
	ds_read_b128 v[92:95], v40
	v_mfma_f32_16x16x32_f16 v[32:35], v[104:107], v[116:119], v[32:35]
	s_waitcnt lgkmcnt(1)
	v_mfma_f32_16x16x32_f16 v[104:107], v[120:123], v[88:91], v[24:27]
	s_nop 2
	v_or_b32_e32 v24, 0x19000, v58
	v_mfma_f32_16x16x32_f16 v[116:119], v[124:127], v[88:91], v[36:39]
	v_mfma_f32_16x16x32_f16 v[76:79], v[88:91], v[128:131], v[76:79]
	s_waitcnt lgkmcnt(0)
	v_mfma_f32_16x16x32_f16 v[88:91], v[120:123], v[92:95], v[28:31]
	v_mfma_f32_16x16x32_f16 v[84:87], v[124:127], v[92:95], v[84:87]
	v_mfma_f32_16x16x32_f16 v[92:95], v[92:95], v[128:131], v[20:23]
	s_nop 2
	ds_read_b128 v[20:23], v24
	v_or_b32_e32 v24, 0x19800, v58
	ds_read_b128 v[24:27], v24
	s_waitcnt lgkmcnt(1)
	v_mfma_f32_16x16x32_f16 v[60:63], v[120:123], v[20:23], v[60:63]
	v_mfma_f32_16x16x32_f16 v[72:75], v[124:127], v[20:23], v[72:75]
	v_mfma_f32_16x16x32_f16 v[136:139], v[20:23], v[128:131], v[32:35]
	s_waitcnt lgkmcnt(0)
	v_mfma_f32_16x16x32_f16 v[64:67], v[120:123], v[24:27], v[64:67]
	v_mfma_f32_16x16x32_f16 v[68:71], v[124:127], v[24:27], v[68:71]
	v_mfma_f32_16x16x32_f16 v[80:83], v[24:27], v[128:131], v[80:83]
	v_add_co_u32_e32 v18, vcc, s2, v18
	s_mov_b32 s2, 0x3c800000
	s_nop 0
	v_addc_co_u32_e32 v19, vcc, 0, v19, vcc
	s_nop 0
	s_waitcnt vmcnt(12)
	v_mov_b32_e32 v50, v200
	v_mov_b32_e32 v51, v201
	v_mov_b32_e32 v52, v202
	v_mov_b32_e32 v53, v203
	v_mov_b32_e32 v96, v204
	v_mov_b32_e32 v97, v205
	v_mov_b32_e32 v98, v206
	v_mov_b32_e32 v99, v207
	v_mov_b32_e32 v100, v208
	v_mov_b32_e32 v101, v209
	v_mov_b32_e32 v102, v210
	v_mov_b32_e32 v103, v211
	v_mov_b32_e32 v108, v212
	v_mov_b32_e32 v109, v213
	v_mov_b32_e32 v110, v214
	v_mov_b32_e32 v111, v215
	v_mov_b32_e32 v112, v216
	v_mov_b32_e32 v113, v217
	v_mov_b32_e32 v114, v218
	v_mov_b32_e32 v115, v219
	v_mov_b32_e32 v132, v220
	v_mov_b32_e32 v133, v221
	v_mov_b32_e32 v134, v222
	v_mov_b32_e32 v135, v223

.Lproj_go_13:
	ds_read_b128 v[120:123], v59
	v_or_b32_e32 v59, 0x1a800, v57
	ds_read_b128 v[124:127], v59
	v_or_b32_e32 v59, 0x1b000, v57
	s_waitcnt lgkmcnt(1)
	v_mfma_f32_16x16x32_f16 v[104:107], v[50:53], v[120:123], v[104:107]
	v_mfma_f32_16x16x32_f16 v[116:119], v[96:99], v[120:123], v[116:119]
	v_mfma_f32_16x16x32_f16 v[76:79], v[120:123], v[100:103], v[76:79]
	ds_read_b128 v[120:123], v59
	v_or_b32_e32 v59, 0x1b800, v57
	s_waitcnt lgkmcnt(1)
	v_mfma_f32_16x16x32_f16 v[88:91], v[50:53], v[124:127], v[88:91]
	v_mfma_f32_16x16x32_f16 v[84:87], v[96:99], v[124:127], v[84:87]
	v_mfma_f32_16x16x32_f16 v[92:95], v[124:127], v[100:103], v[92:95]
	ds_read_b128 v[124:127], v59
	v_or_b32_e32 v59, 0x1a000, v58
	s_waitcnt lgkmcnt(1)
	v_mfma_f32_16x16x32_f16 v[60:63], v[50:53], v[120:123], v[60:63]
	s_waitcnt lgkmcnt(0)
	v_mfma_f32_16x16x32_f16 v[50:53], v[50:53], v[124:127], v[64:67]
	v_mfma_f32_16x16x32_f16 v[64:67], v[96:99], v[124:127], v[68:71]
	v_mfma_f32_16x16x32_f16 v[68:71], v[124:127], v[100:103], v[80:83]
	v_or_b32_e32 v124, 0x1d800, v58
	s_nop 1
	ds_read_b128 v[80:83], v59
	v_or_b32_e32 v59, 0x1a800, v58
	v_mfma_f32_16x16x32_f16 v[72:75], v[96:99], v[120:123], v[72:75]
	ds_read_b128 v[96:99], v59
	v_or_b32_e32 v59, 0x1b000, v58
	v_mfma_f32_16x16x32_f16 v[120:123], v[120:123], v[100:103], v[136:139]
	s_waitcnt lgkmcnt(1)
	v_mfma_f32_16x16x32_f16 v[100:103], v[108:111], v[80:83], v[104:107]
	v_mfma_f32_16x16x32_f16 v[104:107], v[112:115], v[80:83], v[116:119]
	v_mfma_f32_16x16x32_f16 v[76:79], v[80:83], v[132:135], v[76:79]
	s_waitcnt lgkmcnt(0)
	v_mfma_f32_16x16x32_f16 v[80:83], v[108:111], v[96:99], v[88:91]
	v_mfma_f32_16x16x32_f16 v[88:91], v[96:99], v[132:135], v[92:95]
	s_nop 2
	ds_read_b128 v[92:95], v59
	v_or_b32_e32 v59, 0x1b800, v58
	v_mfma_f32_16x16x32_f16 v[84:87], v[112:115], v[96:99], v[84:87]
	ds_read_b128 v[96:99], v59
	v_or_b32_e32 v59, 0x1c000, v57
	s_waitcnt lgkmcnt(0)
	v_mfma_f32_16x16x32_f16 v[60:63], v[108:111], v[92:95], v[60:63]
	s_waitcnt vmcnt(6)
	v_mov_b32_e32 v46, v224
	v_mov_b32_e32 v47, v225
	v_mov_b32_e32 v48, v226
	v_mov_b32_e32 v49, v227
	v_mov_b32_e32 v42, v228
	v_mov_b32_e32 v43, v229
	v_mov_b32_e32 v44, v230
	v_mov_b32_e32 v45, v231
	v_mov_b32_e32 v14, v232
	v_mov_b32_e32 v15, v233
	v_mov_b32_e32 v16, v234
	v_mov_b32_e32 v17, v235
	v_mov_b32_e32 v10, v236
	v_mov_b32_e32 v11, v237
	v_mov_b32_e32 v12, v238
	v_mov_b32_e32 v13, v239
	v_mov_b32_e32 v6, v240
	v_mov_b32_e32 v7, v241
	v_mov_b32_e32 v8, v242
	v_mov_b32_e32 v9, v243
	v_mov_b32_e32 v2, v244
	v_mov_b32_e32 v3, v245
	v_mov_b32_e32 v4, v246
	v_mov_b32_e32 v5, v247

.Lproj_go_14:
	v_mfma_f32_16x16x32_f16 v[108:111], v[108:111], v[96:99], v[50:53]
	v_mfma_f32_16x16x32_f16 v[50:53], v[96:99], v[132:135], v[68:71]
	s_nop 2
	ds_read_b128 v[68:71], v59
	v_or_b32_e32 v59, 0x1c800, v57
	v_mfma_f32_16x16x32_f16 v[64:67], v[112:115], v[96:99], v[64:67]
	ds_read_b128 v[96:99], v59
	v_or_b32_e32 v59, 0x1d000, v57
	v_mfma_f32_16x16x32_f16 v[72:75], v[112:115], v[92:95], v[72:75]
	v_or_b32_e32 v112, 0x1d800, v57
	v_mfma_f32_16x16x32_f16 v[92:95], v[92:95], v[132:135], v[120:123]
	v_or_b32_e32 v132, 0x1e800, v57
	s_waitcnt lgkmcnt(1)
	v_mfma_f32_16x16x32_f16 v[100:103], v[46:49], v[68:71], v[100:103]
	v_or_b32_e32 v120, 0x1c800, v58
	v_mfma_f32_16x16x32_f16 v[104:107], v[42:45], v[68:71], v[104:107]
	v_mfma_f32_16x16x32_f16 v[68:71], v[68:71], v[14:17], v[76:79]
	s_waitcnt lgkmcnt(0)
	v_mfma_f32_16x16x32_f16 v[76:79], v[46:49], v[96:99], v[80:83]
	s_nop 2
	ds_read_b128 v[80:83], v59
	ds_read_b128 v[112:115], v112
	v_or_b32_e32 v59, 0x1c000, v58
	ds_read_b128 v[116:119], v59
	ds_read_b128 v[120:123], v120
	v_or_b32_e32 v59, 0x1d000, v58
	v_mfma_f32_16x16x32_f16 v[84:87], v[42:45], v[96:99], v[84:87]
	v_mfma_f32_16x16x32_f16 v[88:91], v[96:99], v[14:17], v[88:91]
	ds_read_b128 v[96:99], v59
	ds_read_b128 v[124:127], v124
	v_or_b32_e32 v59, 0x1e000, v57
	s_waitcnt lgkmcnt(0)
	s_waitcnt vmcnt(0)
	v_mov_b32_e32 v38, v176
	v_mov_b32_e32 v39, v177
	v_mov_b32_e32 v40, v178
	v_mov_b32_e32 v41, v179
	v_mov_b32_e32 v34, v180
	v_mov_b32_e32 v35, v181
	v_mov_b32_e32 v36, v182
	v_mov_b32_e32 v37, v183
	v_mov_b32_e32 v30, v184
	v_mov_b32_e32 v31, v185
	v_mov_b32_e32 v32, v186
	v_mov_b32_e32 v33, v187
	v_mov_b32_e32 v22, v188
	v_mov_b32_e32 v23, v189
	v_mov_b32_e32 v24, v190
	v_mov_b32_e32 v25, v191
	v_mov_b32_e32 v26, v192
	v_mov_b32_e32 v27, v193
	v_mov_b32_e32 v28, v194
	v_mov_b32_e32 v29, v195
	v_mov_b32_e32 v18, v196
	v_mov_b32_e32 v19, v197
	v_mov_b32_e32 v20, v198
	v_mov_b32_e32 v21, v199

.Lproj_go_15:
	v_mfma_f32_16x16x32_f16 v[100:103], v[10:13], v[116:119], v[100:103]
	ds_read_b128 v[128:131], v59
	ds_read_b128 v[132:135], v132
	v_or_b32_e32 v59, 0x1f000, v57
	v_or_b32_e32 v57, 0x1f800, v57
	v_mfma_f32_16x16x32_f16 v[104:107], v[6:9], v[116:119], v[104:107]
	ds_read_b128 v[136:139], v59
	ds_read_b128 v[140:143], v57
	v_or_b32_e32 v57, 0x1e000, v58
	v_or_b32_e32 v59, 0x1e800, v58
	v_mfma_f32_16x16x32_f16 v[68:71], v[116:119], v[2:5], v[68:71]
	ds_read_b128 v[116:119], v57
	ds_read_b128 v[144:147], v59
	v_or_b32_e32 v57, 0x1f000, v58
	v_or_b32_e32 v58, 0x1f800, v58
	s_waitcnt lgkmcnt(5)
	v_mfma_f32_16x16x32_f16 v[100:103], v[38:41], v[128:131], v[100:103]
	ds_read_b128 v[148:151], v57
	ds_read_b128 v[152:155], v58
	v_lshl_add_u64 v[58:59], s[4:5], 0, v[54:55]
	v_and_b32_e32 v54, 48, v0
	v_mfma_f32_16x16x32_f16 v[104:107], v[34:37], v[128:131], v[104:107]
	s_lshl_b32 s4, s16, 5
	v_mfma_f32_16x16x32_f16 v[68:71], v[128:131], v[30:33], v[68:71]
	v_lshl_add_u64 v[128:129], v[58:59], 0, v[54:55]
	s_waitcnt lgkmcnt(3)
	v_mfma_f32_16x16x32_f16 v[100:103], v[22:25], v[116:119], v[100:103]
	v_mfma_f32_16x16x32_f16 v[104:107], v[26:29], v[116:119], v[104:107]
	v_mfma_f32_16x16x32_f16 v[68:71], v[116:119], v[18:21], v[68:71]
	s_nop 3
	v_mov_b32_e32 v54, v101
	v_mov_b32_e32 v55, v102
	v_pk_mul_f32 v[54:55], v[54:55], s[2:3] op_sel_hi:[1,0]
	v_mfma_f32_16x16x32_f16 v[76:79], v[10:13], v[120:123], v[76:79]
	v_fma_mixlo_f16 v57, v100, s2, 0
	v_cvt_pk_f16_f32 v100, v54, v55
	v_mov_b32_e32 v54, v105
	v_mov_b32_e32 v55, v106
	v_mfma_f32_16x16x32_f16 v[84:87], v[6:9], v[120:123], v[84:87]
	v_mul_f32_e64 v54, v54, s2
	v_mul_f32_e64 v55, v55, s2
	v_pack_b32_f16 v58, v57, v100
	v_cvt_pk_f16_f32 v57, v54, v55
	v_mov_b32_e32 v54, v69
	v_mfma_f32_16x16x32_f16 v[88:91], v[120:123], v[2:5], v[88:91]
	v_mov_b32_e32 v55, v70
	v_pk_mul_f32 v[54:55], v[54:55], s[2:3] op_sel_hi:[1,0]
	v_fma_mixlo_f16 v59, v104, s2, 0
	v_mfma_f32_16x16x32_f16 v[76:79], v[38:41], v[132:135], v[76:79]
	v_cvt_pk_f16_f32 v70, v54, v55
	v_fma_mixlo_f16 v54, v103, s2, 0
	v_fma_mixlo_f16 v104, v68, s2, 0
	v_mfma_f32_16x16x32_f16 v[84:87], v[34:37], v[132:135], v[84:87]
	v_pack_b32_f16 v68, v59, v57
	v_alignbit_b32 v59, v54, v100, 16
	v_fma_mixlo_f16 v54, v107, s2, 0
	v_alignbit_b32 v69, v54, v57, 16
	v_lshlrev_b64 v[100:101], 7, v[156:157]
	v_mfma_f32_16x16x32_f16 v[88:91], v[132:135], v[30:33], v[88:91]
	v_lshl_or_b32 v105, v56, 3, s4
	v_or_b32_e32 v100, v100, v105
	v_lshl_add_u64 v[102:103], s[6:7], 0, v[100:101]
	s_waitcnt lgkmcnt(2)
	v_mfma_f32_16x16x32_f16 v[54:57], v[22:25], v[144:147], v[76:79]
	v_subrev_u32_e32 v170, s21, v102
	ds_write_b64 v170, v[58:59]
	v_lshl_add_u64 v[58:59], s[8:9], 0, v[100:101]
	v_subrev_u32_e32 v170, s22, v58
	ds_write_b64 v170, v[68:69]
	v_mfma_f32_16x16x32_f16 v[76:79], v[26:29], v[144:147], v[84:87]
	v_or_b32_e32 v68, 16, v156
	s_nop 2
	v_fma_mixlo_f16 v58, v54, s2, 0
	v_mov_b32_e32 v54, v55
	v_mfma_f32_16x16x32_f16 v[84:87], v[144:147], v[18:21], v[88:91]
	v_mov_b32_e32 v55, v56
	v_pk_mul_f32 v[54:55], v[54:55], s[2:3] op_sel_hi:[1,0]
	v_fma_mixlo_f16 v59, v76, s2, 0
	v_mfma_f32_16x16x32_f16 v[60:63], v[46:49], v[80:83], v[60:63]
	v_cvt_pk_f16_f32 v56, v54, v55
	v_mov_b32_e32 v54, v77
	v_mov_b32_e32 v55, v78
	v_mfma_f32_16x16x32_f16 v[72:75], v[42:45], v[80:83], v[72:75]
	v_mul_f32_e64 v54, v54, s2
	v_mul_f32_e64 v55, v55, s2
	v_pack_b32_f16 v76, v58, v56
	v_ashrrev_i32_e32 v69, 31, v68
	v_mfma_f32_16x16x32_f16 v[80:83], v[80:83], v[14:17], v[92:95]
	v_lshlrev_b64 v[68:69], 7, v[68:69]
	v_or_b32_e32 v68, v68, v105
	v_fma_mixlo_f16 v84, v84, s2, 0
	v_mfma_f32_16x16x32_f16 v[42:45], v[42:45], v[112:115], v[64:67]
	s_nop 2
	v_cvt_pk_f16_f32 v67, v54, v55
	v_mov_b32_e32 v54, v85
	v_mov_b32_e32 v55, v86
	v_pk_mul_f32 v[54:55], v[54:55], s[2:3] op_sel_hi:[1,0]
	v_pack_b32_f16 v66, v59, v67
	v_mfma_f32_16x16x32_f16 v[58:61], v[10:13], v[96:99], v[60:63]
	v_mfma_f32_16x16x32_f16 v[62:65], v[6:9], v[96:99], v[72:75]
	s_nop 2
	v_cvt_pk_f16_f32 v74, v54, v55
	v_fma_mixlo_f16 v54, v57, s2, 0
	v_alignbit_b32 v77, v54, v56, 16
	v_mfma_f32_16x16x32_f16 v[54:57], v[96:99], v[2:5], v[80:83]
	v_fma_mixlo_f16 v72, v79, s2, 0
	v_alignbit_b32 v67, v72, v67, 16
	v_lshl_add_u64 v[72:73], s[6:7], 0, v[68:69]
	v_mfma_f32_16x16x32_f16 v[46:49], v[46:49], v[112:115], v[108:111]
	v_lshl_add_u64 v[68:69], s[8:9], 0, v[68:69]
	v_subrev_u32_e32 v170, s22, v68
	ds_write_b64 v170, v[66:67]
	v_lshrrev_b32_e32 v67, 16, v70
	v_mfma_f32_16x16x32_f16 v[58:61], v[38:41], v[136:139], v[58:61]
	v_lshrrev_b32_e32 v69, 16, v74
	v_fma_mixhi_f16 v69, v87, s2, 0
	v_fma_mixhi_f16 v67, v71, s2, 0
	v_mfma_f32_16x16x32_f16 v[54:57], v[136:139], v[30:33], v[54:57]
	v_pack_b32_f16 v68, v84, v74
	v_pack_b32_f16 v66, v104, v70
	v_subrev_u32_e32 v170, s23, v128
	ds_write_b128 v170, v[66:69]
	v_mfma_f32_16x16x32_f16 v[62:65], v[34:37], v[136:139], v[62:65]
	v_subrev_u32_e32 v170, s21, v72
	ds_write_b64 v170, v[76:77]
	v_or_b32_e32 v66, 32, v156
	v_ashrrev_i32_e32 v67, 31, v66
	v_mfma_f32_16x16x32_f16 v[14:17], v[112:115], v[14:17], v[50:53]
	v_mfma_f32_16x16x32_f16 v[6:9], v[6:9], v[124:127], v[42:45]
	s_waitcnt lgkmcnt(1)
	v_mfma_f32_16x16x32_f16 v[58:61], v[22:25], v[148:151], v[58:61]
	v_mfma_f32_16x16x32_f16 v[54:57], v[148:151], v[18:21], v[54:57]
	v_mfma_f32_16x16x32_f16 v[10:13], v[10:13], v[124:127], v[46:49]
	s_nop 5
	v_fma_mixlo_f16 v68, v58, s2, 0
	v_mov_b32_e32 v58, v59
	v_mov_b32_e32 v59, v60
	v_mfma_f32_16x16x32_f16 v[62:65], v[26:29], v[148:151], v[62:65]
	v_mul_f32_e64 v50, v58, s2
	v_mul_f32_e64 v51, v59, s2
	v_fma_mixlo_f16 v54, v54, s2, 0
	v_cvt_pk_f16_f32 v50, v50, v51
	v_mfma_f32_16x16x32_f16 v[2:5], v[124:127], v[2:5], v[14:17]
	v_pack_b32_f16 v46, v68, v50
	s_nop 1
	v_mov_b32_e32 v48, v63
	v_mov_b32_e32 v49, v64
	v_mfma_f32_16x16x32_f16 v[6:9], v[34:37], v[140:143], v[6:9]
	v_mov_b32_e32 v14, v55
	v_mov_b32_e32 v15, v56
	v_pk_mul_f32 v[14:15], v[14:15], s[2:3] op_sel_hi:[1,0]
	v_mfma_f32_16x16x32_f16 v[10:13], v[38:41], v[140:143], v[10:13]
	v_mul_f32_e64 v42, v48, s2
	v_mul_f32_e64 v43, v49, s2
	v_cvt_pk_f16_f32 v38, v14, v15
	v_fma_mixlo_f16 v14, v61, s2, 0
	v_mfma_f32_16x16x32_f16 v[2:5], v[140:143], v[30:33], v[2:5]
	v_fma_mixlo_f16 v62, v62, s2, 0
	v_cvt_pk_f16_f32 v43, v42, v43
	v_alignbit_b32 v47, v14, v50, 16
	v_fma_mixlo_f16 v14, v65, s2, 0
	s_waitcnt lgkmcnt(0)
	v_mfma_f32_16x16x32_f16 v[6:9], v[26:29], v[152:155], v[6:9]
	v_pack_b32_f16 v42, v62, v43
	v_alignbit_b32 v43, v14, v43, 16
	v_lshlrev_b64 v[14:15], 7, v[66:67]
	v_mfma_f32_16x16x32_f16 v[10:13], v[22:25], v[152:155], v[10:13]
	v_or_b32_e32 v14, v14, v105
	v_lshl_add_u64 v[16:17], s[6:7], 0, v[14:15]
	v_subrev_u32_e32 v170, s21, v16
	ds_write_b64 v170, v[46:47]
	v_mfma_f32_16x16x32_f16 v[2:5], v[152:155], v[18:21], v[2:5]
	v_lshl_add_u64 v[14:15], s[8:9], 0, v[14:15]
	v_fma_mixlo_f16 v17, v6, s2, 0
	v_mov_b32_e32 v6, v7
	v_mov_b32_e32 v7, v8
	v_subrev_u32_e32 v170, s22, v14
	ds_write_b64 v170, v[42:43]
	v_or_b32_e32 v14, 48, v156
	v_fma_mixlo_f16 v16, v10, s2, 0
	v_mov_b32_e32 v10, v11
	v_mov_b32_e32 v11, v12
	v_pk_mul_f32 v[6:7], v[6:7], s[2:3] op_sel_hi:[1,0]
	v_ashrrev_i32_e32 v15, 31, v14
	v_pk_mul_f32 v[10:11], v[10:11], s[2:3] op_sel_hi:[1,0]
	v_cvt_pk_f16_f32 v7, v6, v7
	v_fma_mixlo_f16 v8, v9, s2, 0
	v_cvt_pk_f16_f32 v12, v10, v11
	v_pack_b32_f16 v6, v17, v7
	v_mov_b32_e32 v10, v3
	v_mov_b32_e32 v11, v4
	v_alignbit_b32 v7, v8, v7, 16
	v_lshlrev_b64 v[8:9], 7, v[14:15]
	v_pk_mul_f32 v[10:11], v[10:11], s[2:3] op_sel_hi:[1,0]
	v_fma_mixlo_f16 v3, v13, s2, 0
	v_or_b32_e32 v8, v8, v105
	v_fma_mixlo_f16 v18, v2, s2, 0
	v_pack_b32_f16 v2, v16, v12
	v_cvt_pk_f16_f32 v4, v10, v11
	v_alignbit_b32 v3, v3, v12, 16
	v_lshl_add_u64 v[10:11], s[6:7], 0, v[8:9]
	v_subrev_u32_e32 v170, s21, v10
	ds_write_b64 v170, v[2:3]
	v_lshl_add_u64 v[2:3], s[8:9], 0, v[8:9]
	v_subrev_u32_e32 v170, s22, v2
	ds_write_b64 v170, v[6:7]
	v_lshrrev_b32_e32 v7, 16, v38
	v_lshrrev_b32_e32 v9, 16, v4
	v_fma_mixhi_f16 v9, v5, s2, 0
	v_fma_mixhi_f16 v7, v57, s2, 0
	v_pack_b32_f16 v8, v18, v4
	v_pack_b32_f16 v6, v54, v38
	v_subrev_u32_e32 v170, s23, v128
	ds_write_b128 v170, v[6:9] offset:64
	s_waitcnt lgkmcnt(0)
	s_barrier
	v_and_b32_e32 v170, 63, v0
	v_lshlrev_b32_e32 v170, 4, v170
	v_lshl_add_u32 v170, s16, 10, v170
	v_add_u32_e32 v168, s24, v170
	v_add_u32_e32 v169, 0x1000, v168
	v_add_u32_e32 v170, 0x20100, v170
	ds_read_b128 v[160:163], v170
	ds_read_b128 v[164:167], v170 offset:4096
	ds_read_b128 v[172:175], v170 offset:8192
	s_waitcnt lgkmcnt(2)
	global_store_dwordx4 v168, v[160:163], s[6:7] sc1
	s_waitcnt lgkmcnt(1)
	global_store_dwordx4 v169, v[164:167], s[6:7] sc1
	s_waitcnt lgkmcnt(0)
	global_store_dwordx4 v168, v[172:175], s[8:9] sc1
	s_nop 1
	ds_read_b128 v[160:163], v170 offset:12288
	ds_read_b128 v[164:167], v170 offset:16384
	ds_read_b128 v[172:175], v170 offset:20480
	s_waitcnt lgkmcnt(2)
	global_store_dwordx4 v169, v[160:163], s[8:9] sc1
	s_waitcnt lgkmcnt(1)
	global_store_dwordx4 v168, v[164:167], s[10:11] sc1
	s_waitcnt lgkmcnt(0)
	global_store_dwordx4 v169, v[172:175], s[10:11] sc1
	s_endpgm

	.amdhsa_kernel _Z11proj_kernelPKfPKDv8_DF16_PDF16_S4_S4_
		.amdhsa_group_segment_fixed_size 155904
		.amdhsa_private_segment_fixed_size 0
		.amdhsa_kernarg_size 40
		.amdhsa_user_sgpr_count 2
		.amdhsa_user_sgpr_dispatch_ptr 0
		.amdhsa_user_sgpr_queue_ptr 0
		.amdhsa_user_sgpr_kernarg_segment_ptr 1
		.amdhsa_user_sgpr_dispatch_id 0
		.amdhsa_user_sgpr_kernarg_preload_length 0
		.amdhsa_user_sgpr_kernarg_preload_offset 0
		.amdhsa_user_sgpr_private_segment_size 0
		.amdhsa_uses_dynamic_stack 0
		.amdhsa_enable_private_segment 0
		.amdhsa_system_sgpr_workgroup_id_x 1
		.amdhsa_system_sgpr_workgroup_id_y 0
		.amdhsa_system_sgpr_workgroup_id_z 0
		.amdhsa_system_sgpr_workgroup_info 0
		.amdhsa_system_vgpr_workitem_id 0
		.amdhsa_next_free_vgpr 256
		.amdhsa_next_free_sgpr 96
		.amdhsa_accum_offset 256
		.amdhsa_reserve_vcc 1
		.amdhsa_float_round_mode_32 0
		.amdhsa_float_round_mode_16_64 0
		.amdhsa_float_denorm_mode_32 3
		.amdhsa_float_denorm_mode_16_64 3
		.amdhsa_dx10_clamp 1
		.amdhsa_ieee_mode 1
		.amdhsa_fp16_overflow 0
		.amdhsa_tg_split 0
		.amdhsa_exception_fp_ieee_invalid_op 0
		.amdhsa_exception_fp_denorm_src 0
		.amdhsa_exception_fp_ieee_div_zero 0
		.amdhsa_exception_fp_ieee_overflow 0
		.amdhsa_exception_fp_ieee_underflow 0
		.amdhsa_exception_fp_ieee_inexact 0
		.amdhsa_exception_int_div_zero 0
	.end_amdhsa_kernel

amdhsa.kernels:
  - .agpr_count:     0
    .args:
      - .actual_access:  read_only
        .address_space:  global
        .offset:         0
        .size:           8
        .value_kind:     global_buffer
      - .actual_access:  read_only
        .address_space:  global
        .offset:         8
        .size:           8
        .value_kind:     global_buffer
      - .actual_access:  read_only
        .address_space:  global
        .offset:         16
        .size:           8
        .value_kind:     global_buffer
      - .actual_access:  write_only
        .address_space:  global
        .offset:         24
        .size:           8
        .value_kind:     global_buffer
      - .offset:         32
        .size:           4
        .value_kind:     hidden_block_count_x
      - .offset:         36
        .size:           4
        .value_kind:     hidden_block_count_y
      - .offset:         40
        .size:           4
        .value_kind:     hidden_block_count_z
      - .offset:         44
        .size:           2
        .value_kind:     hidden_group_size_x
      - .offset:         46
        .size:           2
        .value_kind:     hidden_group_size_y
      - .offset:         48
        .size:           2
        .value_kind:     hidden_group_size_z
      - .offset:         50
        .size:           2
        .value_kind:     hidden_remainder_x
      - .offset:         52
        .size:           2
        .value_kind:     hidden_remainder_y
      - .offset:         54
        .size:           2
        .value_kind:     hidden_remainder_z
      - .offset:         72
        .size:           8
        .value_kind:     hidden_global_offset_x
      - .offset:         80
        .size:           8
        .value_kind:     hidden_global_offset_y
      - .offset:         88
        .size:           8
        .value_kind:     hidden_global_offset_z
      - .offset:         96
        .size:           2
        .value_kind:     hidden_grid_dims
    .group_segment_fixed_size: 0
    .kernarg_segment_align: 8
    .kernarg_segment_size: 288
    .language:       OpenCL C
    .language_version:
      - 2
      - 0
    .max_flat_workgroup_size: 1024
    .name:           _Z13prep_w_kernelPKfS0_S0_PDv8_DF16_
    .private_segment_fixed_size: 0
    .sgpr_count:     18
    .sgpr_spill_count: 0
    .symbol:         _Z13prep_w_kernelPKfS0_S0_PDv8_DF16_.kd
    .uniform_work_group_size: 1
    .uses_dynamic_stack: false
    .vgpr_count:     15
    .vgpr_spill_count: 0
    .wavefront_size: 64
  - .agpr_count:     0
    .args:
      - .actual_access:  read_only
        .address_space:  global
        .offset:         0
        .size:           8
        .value_kind:     global_buffer
      - .actual_access:  read_only
        .address_space:  global
        .offset:         8
        .size:           8
        .value_kind:     global_buffer
      - .actual_access:  write_only
        .address_space:  global
        .offset:         16
        .size:           8
        .value_kind:     global_buffer
      - .actual_access:  write_only
        .address_space:  global
        .offset:         24
        .size:           8
        .value_kind:     global_buffer
      - .actual_access:  write_only
        .address_space:  global
        .offset:         32
        .size:           8
        .value_kind:     global_buffer
    .group_segment_fixed_size: 155904
    .kernarg_segment_align: 8
    .kernarg_segment_size: 40
    .language:       OpenCL C
    .language_version:
      - 2
      - 0
    .max_flat_workgroup_size: 512
    .name:           _Z11proj_kernelPKfPKDv8_DF16_PDF16_S4_S4_
    .private_segment_fixed_size: 0
    .sgpr_count:     26
    .sgpr_spill_count: 0
    .symbol:         _Z11proj_kernelPKfPKDv8_DF16_PDF16_S4_S4_.kd
    .uniform_work_group_size: 1
    .uses_dynamic_stack: false
    .vgpr_count:     256
    .vgpr_spill_count: 0
    .wavefront_size: 64
  - .agpr_count:     0
    .args:
      - .actual_access:  read_only
        .address_space:  global
        .offset:         0
        .size:           8
        .value_kind:     global_buffer
      - .address_space:  global
        .offset:         8
        .size:           8
        .value_kind:     global_buffer
      - .address_space:  global
        .offset:         16
        .size:           8
        .value_kind:     global_buffer
      - .actual_access:  write_only
        .address_space:  global
        .offset:         24
        .size:           8
        .value_kind:     global_buffer
      - .actual_access:  write_only
        .address_space:  global
        .offset:         32
        .size:           8
        .value_kind:     global_buffer
      - .actual_access:  write_only
        .address_space:  global
        .offset:         40
        .size:           8
        .value_kind:     global_buffer
    .group_segment_fixed_size: 65536
    .kernarg_segment_align: 8
    .kernarg_segment_size: 48
    .language:       OpenCL C
    .language_version:
      - 2
      - 0
    .max_flat_workgroup_size: 512
    .name:           _Z11attn_kernelPKDF16_S0_S0_PfPDF16_S1_
    .private_segment_fixed_size: 0
    .sgpr_count:     96
    .sgpr_spill_count: 0
    .symbol:         _Z11attn_kernelPKDF16_S0_S0_PfPDF16_S1_.kd
    .uniform_work_group_size: 1
    .uses_dynamic_stack: false
    .vgpr_count:     120
    .vgpr_spill_count: 0
    .wavefront_size: 64
  - .agpr_count:     0
    .args:
      - .actual_access:  read_only
        .address_space:  global
        .offset:         0
        .size:           8
        .value_kind:     global_buffer
      - .actual_access:  read_only
        .address_space:  global
        .offset:         8
        .size:           8
        .value_kind:     global_buffer
      - .actual_access:  write_only
        .address_space:  global
        .offset:         16
        .size:           8
        .value_kind:     global_buffer
    .group_segment_fixed_size: 0
    .kernarg_segment_align: 8
    .kernarg_segment_size: 24
    .language:       OpenCL C
    .language_version:
      - 2
      - 0
    .max_flat_workgroup_size: 256
    .name:           _Z14combine_kernelPKDF16_PKfPf
    .private_segment_fixed_size: 0
    .sgpr_count:     70
    .sgpr_spill_count: 0
    .symbol:         _Z14combine_kernelPKDF16_PKfPf.kd
    .uniform_work_group_size: 1
    .uses_dynamic_stack: false
    .vgpr_count:     46
    .vgpr_spill_count: 0
    .wavefront_size: 64
